# f1 + packed f32 VALU ops (v_pk_mul/add_f32) in the MFMA-interleaved attention and hgrn loops split into scalar pairs (same results, same code size)
# speedup vs baseline: 1.0040x; 1.0012x over previous
.LBB0_890:
	s_or_b64 exec, exec, s[44:45]
	s_waitcnt vmcnt(1)
	v_and_b32_e32 v4, 0xffff0000, v38
	v_lshlrev_b32_e32 v2, 16, v38
	v_mul_f32_e32 v38, v4, v4
	v_lshlrev_b32_e32 v5, 16, v39
	v_fmac_f32_e32 v38, v2, v2
	v_and_b32_e32 v39, 0xffff0000, v39
	v_fmac_f32_e32 v38, v5, v5
	v_lshlrev_b32_e32 v47, 16, v40
	v_fmac_f32_e32 v38, v39, v39
	v_and_b32_e32 v40, 0xffff0000, v40
	v_fmac_f32_e32 v38, v47, v47
	v_lshlrev_b32_e32 v58, 16, v41
	v_fmac_f32_e32 v38, v40, v40
	v_and_b32_e32 v41, 0xffff0000, v41
	v_fmac_f32_e32 v38, v58, v58
	v_fmac_f32_e32 v38, v41, v41
	s_nop 1
	v_add_f32_dpp v38, v38, v38 quad_perm:[1,0,3,2] row_mask:0xf bank_mask:0xf bound_ctrl:1
	s_nop 1
	v_add_f32_dpp v38, v38, v38 quad_perm:[2,3,0,1] row_mask:0xf bank_mask:0xf bound_ctrl:1
	s_nop 1
	v_add_f32_dpp v38, v38, v38 row_half_mirror row_mask:0xf bank_mask:0xf bound_ctrl:1
	s_nop 1
	v_add_f32_dpp v38, v38, v38 row_mirror row_mask:0xf bank_mask:0xf bound_ctrl:1
	v_mov_b32_e32 v59, v38
	s_nop 1
	v_permlane16_swap_b32_e32 v38, v59
	v_add_f32_e32 v38, v38, v59
	v_mov_b32_e32 v59, v38
	s_nop 1
	v_permlane32_swap_b32_e32 v38, v59
	v_add_f32_e32 v38, v38, v59
	v_fmamk_f32 v38, v38, 0x3b000000, v1
	v_mul_f32_e32 v59, 0x4b800000, v38
	v_cmp_gt_f32_e32 vcc, s53, v38
	s_nop 1
	v_cndmask_b32_e32 v38, v38, v59, vcc
	v_rsq_f32_e32 v38, v38
	s_nop 0
	v_mul_f32_e32 v59, 0x45800000, v38
	v_cndmask_b32_e32 v59, v38, v59, vcc
	v_mul_f32_e32 v4, v59, v4
	v_mul_f32_e32 v2, v59, v2
	v_mul_f32_e32 v4, v11, v4
	v_mul_f32_e32 v2, v10, v2
	v_cvt_pk_bf16_f32 v38, v2, v4
	v_mul_f32_e32 v4, v59, v39
	v_mul_f32_e32 v2, v59, v5
	v_mul_f32_e32 v4, v13, v4
	v_mul_f32_e32 v2, v12, v2
	v_cvt_pk_bf16_f32 v39, v2, v4
	v_mul_f32_e32 v4, v59, v40
	v_mul_f32_e32 v2, v59, v47
	v_mul_f32_e32 v4, v7, v4
	v_mul_f32_e32 v2, v6, v2
	v_cvt_pk_bf16_f32 v40, v2, v4
	v_mul_f32_e32 v4, v59, v41
	v_mul_f32_e32 v2, v59, v58
	v_mul_f32_e32 v4, v9, v4
	v_mul_f32_e32 v2, v8, v2
	v_cvt_pk_bf16_f32 v41, v2, v4
	v_lshl_add_u64 v[4:5], s[46:47], 0, v[56:57]
	global_store_dwordx4 v[4:5], v[38:41], off
	v_lshlrev_b32_e32 v4, 16, v44
	v_and_b32_e32 v5, 0xffff0000, v44
	v_and_b32_e32 v41, 0xffff0000, v42
	v_lshlrev_b32_e32 v40, 16, v42
	v_mul_f32_e32 v44, v41, v41
	v_lshlrev_b32_e32 v42, 16, v43
	v_fmac_f32_e32 v44, v40, v40
	v_and_b32_e32 v43, 0xffff0000, v43
	v_add_f32_e32 v2, 0, v40
	v_fmac_f32_e32 v44, v42, v42
	v_add_f32_e32 v2, v2, v41
	v_fmac_f32_e32 v44, v43, v43
	v_add_f32_e32 v2, v2, v42
	v_fmac_f32_e32 v44, v4, v4
	v_lshlrev_b32_e32 v38, 16, v45
	v_add_f32_e32 v2, v2, v43
	v_fmac_f32_e32 v44, v5, v5
	v_and_b32_e32 v39, 0xffff0000, v45
	v_add_f32_e32 v2, v2, v4
	v_fmac_f32_e32 v44, v38, v38
	v_add_f32_e32 v2, v2, v5
	v_fmac_f32_e32 v44, v39, v39
	v_add_f32_e32 v2, v2, v38
	v_cndmask_b32_e64 v44, 0, v44, s[6:7]
	v_add_f32_e32 v2, v2, v39
	v_cndmask_b32_e64 v2, 0, v2, s[14:15]
	v_add_f32_dpp v44, v44, v44 quad_perm:[1,0,3,2] row_mask:0xf bank_mask:0xf bound_ctrl:1
	s_nop 0
	v_add_f32_dpp v2, v2, v2 quad_perm:[1,0,3,2] row_mask:0xf bank_mask:0xf bound_ctrl:1
	v_add_f32_dpp v44, v44, v44 quad_perm:[2,3,0,1] row_mask:0xf bank_mask:0xf bound_ctrl:1
	s_nop 0
	v_add_f32_dpp v2, v2, v2 quad_perm:[2,3,0,1] row_mask:0xf bank_mask:0xf bound_ctrl:1
	v_add_f32_dpp v44, v44, v44 row_half_mirror row_mask:0xf bank_mask:0xf bound_ctrl:1
	s_nop 0
	v_add_f32_dpp v2, v2, v2 row_half_mirror row_mask:0xf bank_mask:0xf bound_ctrl:1
	v_add_f32_dpp v44, v44, v44 row_mirror row_mask:0xf bank_mask:0xf bound_ctrl:1
	v_mov_b32_e32 v45, v44
	s_nop 1
	v_permlane16_swap_b32_e32 v44, v45
	v_add_f32_dpp v2, v2, v2 row_mirror row_mask:0xf bank_mask:0xf bound_ctrl:1
	v_add_f32_e32 v63, v44, v45
	v_mov_b32_e32 v44, v2
	s_nop 1
	v_permlane16_swap_b32_e32 v2, v44
	v_add_f32_e32 v2, v2, v44
	v_mov_b32_e32 v44, v2
	s_nop 1
	v_permlane32_swap_b32_e32 v2, v44
	v_add_f32_e32 v62, v2, v44
	v_fmamk_f32 v44, v62, 0xbc800000, v41
	v_fmamk_f32 v2, v62, 0xbc800000, v40
	v_mul_f32_e32 v65, v44, v44
	v_fmac_f32_e32 v65, v2, v2
	v_fmamk_f32 v45, v62, 0xbc800000, v42
	v_fmac_f32_e32 v65, v45, v45
	v_fmamk_f32 v47, v62, 0xbc800000, v43
	v_fmac_f32_e32 v65, v47, v47
	v_fmamk_f32 v58, v62, 0xbc800000, v4
	v_fmac_f32_e32 v65, v58, v58
	v_fmamk_f32 v59, v62, 0xbc800000, v5
	v_fmac_f32_e32 v65, v59, v59
	v_fmamk_f32 v61, v62, 0xbc800000, v38
	v_fmac_f32_e32 v65, v61, v61
	v_fmamk_f32 v62, v62, 0xbc800000, v39
	v_fmac_f32_e32 v65, v62, v62
	v_cndmask_b32_e64 v65, 0, v65, s[14:15]
	v_mov_b32_e32 v64, v63
	s_nop 1
	v_permlane32_swap_b32_e32 v63, v64
	v_add_f32_dpp v65, v65, v65 quad_perm:[1,0,3,2] row_mask:0xf bank_mask:0xf bound_ctrl:1
	s_nop 1
	v_add_f32_dpp v65, v65, v65 quad_perm:[2,3,0,1] row_mask:0xf bank_mask:0xf bound_ctrl:1
	s_nop 1
	v_add_f32_dpp v65, v65, v65 row_half_mirror row_mask:0xf bank_mask:0xf bound_ctrl:1
	s_nop 1
	v_add_f32_dpp v65, v65, v65 row_mirror row_mask:0xf bank_mask:0xf bound_ctrl:1
	v_mov_b32_e32 v66, v65
	s_nop 1
	v_permlane16_swap_b32_e32 v65, v66
	v_add_f32_e32 v65, v65, v66
	v_mov_b32_e32 v66, v65
	s_nop 1
	v_permlane32_swap_b32_e32 v65, v66
	s_and_saveexec_b64 s[44:45], s[8:9]
	s_xor_b64 s[44:45], exec, s[44:45]
	s_cbranch_execz .LBB0_898
	s_and_saveexec_b64 s[56:57], s[10:11]
	s_xor_b64 s[64:65], exec, s[56:57]
	s_cbranch_execz .LBB0_895
	s_and_saveexec_b64 s[66:67], s[12:13]
	s_cbranch_execz .LBB0_894
	v_lshl_add_u64 v[44:45], s[46:47], 0, v[54:55]
	v_add_co_u32_e32 v44, vcc, 0x30738000, v44
	v_mul_f32_e32 v42, s28, v42
	v_mul_f32_e32 v43, s28, v43
	v_mul_f32_e32 v40, s28, v40
	v_mul_f32_e32 v41, s28, v41
	v_addc_co_u32_e32 v45, vcc, 0, v45, vcc
	global_store_dwordx4 v[44:45], v[40:43], off offset:2304
	s_nop 1
	v_mul_f32_e32 v40, s28, v38
	v_mul_f32_e32 v41, s28, v39
	v_mul_f32_e32 v38, s28, v4
	v_mul_f32_e32 v39, s28, v5
	global_store_dwordx4 v[44:45], v[38:41], off offset:2320

.LBB0_909:
	s_bitcmp1_b32 s17, 0
	s_cselect_b32 s2, 0x3000, 0
	v_add_u32_e32 v63, s2, v55
	ds_read_u16 v36, v63 offset:33792
	ds_read_u16 v37, v63 offset:34048
	ds_read_u16 v38, v63 offset:34816
	ds_read_u16 v67, v63 offset:36608
	ds_read_u16 v51, v63 offset:36096
	s_waitcnt lgkmcnt(4)
	v_cvt_f32_f16_e32 v36, v36
	s_waitcnt lgkmcnt(3)
	v_cvt_f32_f16_e32 v37, v37
	s_waitcnt lgkmcnt(2)
	v_cvt_f32_f16_e32 v38, v38
	s_waitcnt lgkmcnt(1)
	v_cvt_f32_f16_e32 v78, v67
	v_add_f32_e32 v36, 0, v36
	v_add_f32_e32 v36, v36, v37
	ds_read_u16 v37, v63 offset:34304
	v_cndmask_b32_e64 v39, 0, v38, s[10:11]
	v_cndmask_b32_e64 v67, 0, v78, s[12:13]
	s_waitcnt lgkmcnt(1)
	v_cvt_f32_f16_e32 v74, v51
	ds_read_u16 v65, v63 offset:36352
	s_waitcnt lgkmcnt(1)
	v_cvt_f32_f16_e32 v37, v37
	v_cndmask_b32_e64 v51, 0, v74, s[12:13]
	v_add_f32_e32 v36, v36, v37
	ds_read_u16 v37, v63 offset:34560
	s_waitcnt lgkmcnt(1)
	v_cvt_f32_f16_e32 v76, v65
	s_waitcnt lgkmcnt(0)
	v_cvt_f32_f16_e32 v37, v37
	v_cndmask_b32_e64 v65, 0, v76, s[12:13]
	v_add_f32_e32 v36, v36, v37
	v_cndmask_b32_e64 v37, 0, v36, s[8:9]
	v_add_f32_e32 v37, v37, v39
	ds_read_u16 v39, v63 offset:35072
	s_waitcnt lgkmcnt(0)
	v_cvt_f32_f16_e32 v50, v39
	v_cndmask_b32_e64 v39, 0, v50, s[10:11]
	v_add_f32_e32 v37, v37, v39
	ds_read_u16 v39, v63 offset:35328
	s_waitcnt lgkmcnt(0)
	v_cvt_f32_f16_e32 v64, v39
	v_cndmask_b32_e64 v39, 0, v64, s[10:11]
	v_add_f32_e32 v37, v37, v39
	ds_read_u16 v39, v63 offset:35584
	s_waitcnt lgkmcnt(0)
	v_cvt_f32_f16_e32 v66, v39
	v_cndmask_b32_e64 v39, 0, v66, s[10:11]
	v_add_f32_e32 v37, v37, v39
	ds_read_u16 v39, v63 offset:35840
	ds_read_u16 v73, v63 offset:36864
	ds_read_u16 v75, v63 offset:37120
	ds_read_u16 v77, v63 offset:37376
	ds_read_u16 v79, v63 offset:37632
	v_add_u32_e32 v63, v63, v54
	ds_read_u16 v82, v63 offset:33792
	ds_read_u16 v80, v63 offset:37888
	ds_read_u16 v83, v63 offset:34048
	ds_read_u16 v81, v63 offset:38144
	s_waitcnt lgkmcnt(8)
	v_cvt_f32_f16_e32 v72, v39
	s_waitcnt lgkmcnt(0)
	v_lshl_or_b32 v80, v81, 16, v80
	v_cndmask_b32_e64 v39, 0, v72, s[12:13]
	v_add_f32_e32 v36, v36, v38
	v_add_f32_e32 v37, v37, v39
	v_cvt_f32_f16_e32 v38, v73
	v_add_f32_e32 v36, v36, v50
	v_add_f32_e32 v37, v37, v51
	ds_read_u16 v84, v63 offset:34304
	ds_read_u16 v81, v63 offset:38400
	ds_read_u16 v85, v63 offset:38656
	v_add_f32_e32 v36, v36, v64
	v_add_f32_e32 v37, v37, v65
	v_cvt_f32_f16_e32 v64, v75
	v_add_f32_e32 v36, v36, v66
	v_add_f32_e32 v37, v37, v67
	v_cndmask_b32_e64 v73, 0, v38, s[14:15]
	v_cvt_f32_f16_e32 v66, v77
	ds_read_u16 v63, v63 offset:34560
	v_add_f32_e32 v36, v36, v72
	v_add_f32_e32 v37, v37, v73
	v_cvt_f32_f16_e32 v72, v79
	v_cvt_f32_f16_e32 v39, v82
	v_cndmask_b32_e64 v75, 0, v64, s[14:15]
	v_cvt_f32_f16_e32 v65, v83
	v_add_f32_e32 v36, v36, v74
	v_add_f32_e32 v37, v37, v75
	v_cndmask_b32_e64 v77, 0, v66, s[14:15]
	s_waitcnt lgkmcnt(3)
	v_cvt_f32_f16_e32 v67, v84
	v_add_f32_e32 v36, v36, v76
	v_add_f32_e32 v37, v37, v77
	v_cndmask_b32_e64 v79, 0, v72, s[14:15]
	s_waitcnt lgkmcnt(0)
	v_cvt_f32_f16_e32 v73, v63
	v_add_f32_e32 v36, v36, v78
	v_add_f32_e32 v37, v37, v79
	v_lshl_or_b32 v81, v85, 16, v81
	v_add_f32_e32 v36, v36, v38
	v_add_f32_e32 v37, v37, v39
	v_mul_f32_e32 v38, 0x3fb8aa3b, v39
	v_add_f32_e32 v74, v36, v64
	v_add_f32_e32 v75, v37, v65
	v_exp_f32_e32 v38, v38
	v_add_f32_e32 v76, v74, v66
	v_add_f32_e32 v77, v75, v67
	v_mul_f32_e32 v63, 0x3fb8aa3b, v73
	v_add_f32_e32 v50, v76, v72
	v_add_f32_e32 v51, v77, v73
	s_nop 0
	v_sub_f32_e32 v36, v50, v37
	v_mul_f32_e32 v37, 0x3fb8aa3b, v65
	v_exp_f32_e32 v64, v37
	v_sub_f32_e32 v37, v50, v75
	v_mul_f32_e32 v37, 0x3fb8aa3b, v37
	v_exp_f32_e32 v66, v37
	v_mul_f32_e32 v37, 0x3fb8aa3b, v67
	v_exp_f32_e32 v39, v37
	v_sub_f32_e32 v37, v50, v77
	v_mul_f32_e32 v36, 0x3fb8aa3b, v36
	v_mul_f32_e32 v37, 0x3fb8aa3b, v37
	v_exp_f32_e32 v36, v36
	v_exp_f32_e32 v37, v37
	v_sub_f32_e32 v51, v50, v51
	v_exp_f32_e32 v65, v63
	v_mul_f32_e32 v51, 0x3fb8aa3b, v51
	v_exp_f32_e32 v67, v51
	v_pk_add_f32 v[38:39], v[38:39], 1.0 op_sel_hi:[1,0] neg_lo:[1,0] neg_hi:[1,0]
	s_nop 0
	v_mul_f32_e32 v36, v38, v36
	v_mul_f32_e32 v37, v39, v37
	s_nop 0
	v_and_b32_sdwa v38, v37, v60 dst_sel:DWORD dst_unused:UNUSED_PAD src0_sel:WORD_1 src1_sel:DWORD
	v_and_b32_sdwa v39, v36, v60 dst_sel:DWORD dst_unused:UNUSED_PAD src0_sel:WORD_1 src1_sel:DWORD
	v_add3_u32 v39, v36, v39, s52
	v_add3_u32 v38, v37, v38, s52
	v_pk_add_f32 v[36:37], v[64:65], 1.0 op_sel_hi:[1,0] neg_lo:[1,0] neg_hi:[1,0]
	s_nop 0
	v_mul_f32_e32 v36, v36, v66
	v_mul_f32_e32 v37, v37, v67
	s_nop 0
	v_and_b32_sdwa v51, v37, v60 dst_sel:DWORD dst_unused:UNUSED_PAD src0_sel:WORD_1 src1_sel:DWORD
	v_and_b32_sdwa v63, v36, v60 dst_sel:DWORD dst_unused:UNUSED_PAD src0_sel:WORD_1 src1_sel:DWORD
	v_add3_u32 v37, v37, v51, s52
	v_add3_u32 v36, v36, v63, s52
	v_and_b32_e32 v37, 0xffff0000, v37
	v_and_b32_e32 v36, 0xffff0000, v36
	v_or_b32_sdwa v37, v37, v38 dst_sel:DWORD dst_unused:UNUSED_PAD src0_sel:DWORD src1_sel:WORD_1
	v_or_b32_sdwa v36, v36, v39 dst_sel:DWORD dst_unused:UNUSED_PAD src0_sel:DWORD src1_sel:WORD_1
	ds_write2st64_b64 v57, v[36:37], v[80:81] offset0:16 offset1:32
	s_and_saveexec_b64 s[2:3], s[6:7]
	s_cbranch_execz .LBB0_911
	v_mul_f32_e32 v36, 0x3fb8aa3b, v50
	v_exp_f32_e32 v36, v36
	v_add_u32_e32 v37, 0, v52
	ds_write_b32 v37, v36 offset:24576
.LBB0_911:
	s_or_b64 exec, exec, s[2:3]
	s_waitcnt lgkmcnt(0)
	s_barrier
	ds_read_b128 v[36:39], v58 offset:16384
	ds_read_b128 v[64:67], v59 offset:24576
	ds_read_b128 v[72:75], v61 offset:8192
	s_add_i32 s2, s17, 1
	s_bitcmp1_b32 s2, 0
	s_cselect_b32 s3, 0x3000, 0
	s_waitcnt lgkmcnt(1)
	v_mul_f32_e32 v32, v32, v64
	v_mul_f32_e32 v33, v33, v65
	v_mul_f32_e32 v34, v34, v66
	v_mul_f32_e32 v35, v35, v67
	s_cmp_gt_u32 s17, 61
	s_waitcnt lgkmcnt(0)
	v_mfma_f32_16x16x32_bf16 v[32:35], v[72:75], v[36:39], v[32:35]
	ds_read_b128 v[64:67], v59 offset:24640
	ds_read_b128 v[72:75], v61 offset:9216
	s_waitcnt lgkmcnt(1)
	v_mul_f32_e32 v28, v28, v64
	v_mul_f32_e32 v29, v29, v65
	v_mul_f32_e32 v30, v30, v66
	v_mul_f32_e32 v31, v31, v67
	s_waitcnt lgkmcnt(0)
	s_nop 0
	v_mfma_f32_16x16x32_bf16 v[28:31], v[72:75], v[36:39], v[28:31]
	ds_read_b128 v[64:67], v59 offset:24704
	ds_read_b128 v[72:75], v61 offset:10240
	s_waitcnt lgkmcnt(1)
	v_mul_f32_e32 v24, v24, v64
	v_mul_f32_e32 v25, v25, v65
	v_mul_f32_e32 v26, v26, v66
	v_mul_f32_e32 v27, v27, v67
	s_waitcnt lgkmcnt(0)
	s_nop 0
	v_mfma_f32_16x16x32_bf16 v[24:27], v[72:75], v[36:39], v[24:27]
	ds_read_b128 v[64:67], v59 offset:24768
	ds_read_b128 v[72:75], v61 offset:11264
	s_waitcnt lgkmcnt(1)
	v_mul_f32_e32 v20, v20, v64
	v_mul_f32_e32 v21, v21, v65
	v_mul_f32_e32 v22, v22, v66
	v_mul_f32_e32 v23, v23, v67
	s_waitcnt lgkmcnt(0)
	s_nop 0
	v_mfma_f32_16x16x32_bf16 v[20:23], v[72:75], v[36:39], v[20:23]
	ds_read_b128 v[64:67], v59 offset:24832
	ds_read_b128 v[72:75], v61 offset:12288
	s_waitcnt lgkmcnt(1)
	v_mul_f32_e32 v16, v16, v64
	v_mul_f32_e32 v17, v17, v65
	v_mul_f32_e32 v18, v18, v66
	v_mul_f32_e32 v19, v19, v67
	s_waitcnt lgkmcnt(0)
	s_nop 0
	v_mfma_f32_16x16x32_bf16 v[16:19], v[72:75], v[36:39], v[16:19]
	ds_read_b128 v[64:67], v59 offset:24896
	ds_read_b128 v[72:75], v61 offset:13312
	s_waitcnt lgkmcnt(1)
	v_mul_f32_e32 v12, v12, v64
	v_mul_f32_e32 v13, v13, v65
	v_mul_f32_e32 v14, v14, v66
	v_mul_f32_e32 v15, v15, v67
	s_waitcnt lgkmcnt(0)
	s_nop 0
	v_mfma_f32_16x16x32_bf16 v[12:15], v[72:75], v[36:39], v[12:15]
	ds_read_b128 v[64:67], v59 offset:24960
	ds_read_b128 v[72:75], v61 offset:14336
	s_waitcnt lgkmcnt(1)
	v_mul_f32_e32 v8, v8, v64
	v_mul_f32_e32 v9, v9, v65
	v_mul_f32_e32 v10, v10, v66
	v_mul_f32_e32 v11, v11, v67
	s_waitcnt lgkmcnt(0)
	s_nop 0
	v_mfma_f32_16x16x32_bf16 v[8:11], v[72:75], v[36:39], v[8:11]
	ds_read_b128 v[64:67], v59 offset:25024
	ds_read_b128 v[72:75], v61 offset:15360
	s_waitcnt lgkmcnt(1)
	v_mul_f32_e32 v4, v4, v64
	v_mul_f32_e32 v5, v5, v65
	v_mul_f32_e32 v6, v6, v66
	v_mul_f32_e32 v7, v7, v67
	s_waitcnt lgkmcnt(0)
	s_nop 0
	v_mfma_f32_16x16x32_bf16 v[4:7], v[72:75], v[36:39], v[4:7]
	v_add_u32_e32 v36, s3, v53
	s_waitcnt vmcnt(0)
	ds_write2st64_b64 v36, v[46:47], v[48:49] offset0:66 offset1:74
	s_cbranch_scc1 .LBB0_913
	v_lshlrev_b64 v[36:37], 1, v[2:3]
	v_lshl_add_u64 v[38:39], s[30:31], 0, v[36:37]
	v_lshl_add_u64 v[36:37], s[34:35], 0, v[36:37]
	global_load_dwordx2 v[46:47], v[38:39], off
	global_load_dwordx2 v[48:49], v[36:37], off

.LBB0_1973:
	ds_read_b64 v[236:237], v223 offset:448
	v_add_f32_e32 v99, v99, v226
	v_add_f32_e32 v133, v133, v227
	v_add_f32_e32 v149, v149, v230
	v_add_f32_e32 v232, v231, v232
	s_waitcnt lgkmcnt(0)
	v_sub_u32_sdwa v134, s31, v236 dst_sel:DWORD dst_unused:UNUSED_PAD src0_sel:DWORD src1_sel:WORD_0
	v_med3_i32 v134, v134, 0, s24
	v_sub_u32_sdwa v236, s31, v236 dst_sel:DWORD dst_unused:UNUSED_PAD src0_sel:DWORD src1_sel:WORD_1
	v_lshl_add_u32 v134, v134, 6, v154
	v_med3_i32 v236, v236, 0, s24
	ds_read_b32 v134, v134
	v_lshl_add_u32 v236, v236, 6, v154
	s_waitcnt lgkmcnt(0)
	ds_read_b32 v242, v236
	v_sub_u32_sdwa v236, s31, v237 dst_sel:DWORD dst_unused:UNUSED_PAD src0_sel:DWORD src1_sel:WORD_0
	v_med3_i32 v236, v236, 0, s24
	v_lshl_add_u32 v236, v236, 6, v154
	s_waitcnt lgkmcnt(0)
	ds_read_b32 v243, v236
	v_sub_u32_sdwa v236, s31, v237 dst_sel:DWORD dst_unused:UNUSED_PAD src0_sel:DWORD src1_sel:WORD_1
	v_med3_i32 v236, v236, 0, s24
	v_lshl_add_u32 v236, v236, 6, v154
	s_waitcnt lgkmcnt(0)
	ds_read_b32 v244, v236
	s_waitcnt lgkmcnt(0)
	ds_read_b64 v[236:237], v223 offset:480
	v_add_f32_e32 v248, v234, v235
	v_cmp_ge_u32_e32 vcc, s33, v194
	s_addk_i32 s15, 0x100
	s_add_i32 s28, s28, 8
	s_waitcnt lgkmcnt(0)
	v_sub_u32_sdwa v223, s31, v236 dst_sel:DWORD dst_unused:UNUSED_PAD src0_sel:DWORD src1_sel:WORD_0
	v_med3_i32 v223, v223, 0, s24
	v_sub_u32_sdwa v236, s31, v236 dst_sel:DWORD dst_unused:UNUSED_PAD src0_sel:DWORD src1_sel:WORD_1
	v_lshl_add_u32 v223, v223, 6, v154
	v_med3_i32 v236, v236, 0, s24
	ds_read_b32 v223, v223
	v_lshl_add_u32 v236, v236, 6, v154
	s_waitcnt lgkmcnt(0)
	ds_read_b32 v245, v236
	v_add_f32_e32 v236, v224, v225
	v_sub_u32_sdwa v224, s31, v237 dst_sel:DWORD dst_unused:UNUSED_PAD src0_sel:DWORD src1_sel:WORD_0
	v_med3_i32 v224, v224, 0, s24
	v_lshl_add_u32 v224, v224, 6, v154
	s_waitcnt lgkmcnt(0)
	ds_read_b32 v246, v224
	v_sub_u32_sdwa v224, s31, v237 dst_sel:DWORD dst_unused:UNUSED_PAD src0_sel:DWORD src1_sel:WORD_1
	v_med3_i32 v224, v224, 0, s24
	v_lshl_add_u32 v224, v224, 6, v154
	s_waitcnt lgkmcnt(0)
	ds_read_b32 v247, v224
	v_add_f32_e32 v237, v228, v229
	s_waitcnt lgkmcnt(0)
	ds_read_b128 v[224:227], v211
	ds_read_b128 v[228:231], v211 offset:4096
	v_add_f32_e32 v98, v236, v98
	v_fmac_f32_e32 v99, v98, v144
	v_fmac_f32_e32 v133, v99, v132
	v_fmac_f32_e32 v237, v133, v146
	v_fmac_f32_e32 v149, v237, v148
	ds_read_b128 v[234:237], v212
	ds_read_b128 v[238:241], v212 offset:4096
	s_waitcnt lgkmcnt(3)
	v_mfma_f32_16x16x32_bf16 v[224:227], v[224:227], v[94:97], 0
	v_cndmask_b32_e32 v98, v145, v134, vcc
	v_cmp_ge_u32_e32 vcc, s33, v195
	v_fmac_f32_e32 v232, v149, v150
	s_waitcnt lgkmcnt(2)
	v_mfma_f32_16x16x32_bf16 v[94:97], v[228:231], v[94:97], 0
	ds_read_b128 v[228:231], v213
	v_cndmask_b32_e32 v99, v145, v242, vcc
	v_cmp_ge_u32_e32 vcc, s33, v196
	s_waitcnt lgkmcnt(2)
	v_mfma_f32_16x16x32_bf16 v[224:227], v[234:237], v[90:93], v[224:227]
	ds_read_b128 v[234:237], v214
	v_cndmask_b32_e32 v132, v145, v243, vcc
	v_cmp_ge_u32_e32 vcc, s33, v197
	s_waitcnt lgkmcnt(2)
	v_mfma_f32_16x16x32_bf16 v[90:93], v[238:241], v[90:93], v[94:97]
	v_fmac_f32_e32 v248, v232, v152
	v_cndmask_b32_e32 v133, v145, v244, vcc
	v_cmp_ge_u32_e32 vcc, s33, v198
	ds_read_b128 v[94:97], v213 offset:4096
	s_waitcnt lgkmcnt(2)
	v_mfma_f32_16x16x32_bf16 v[224:227], v[228:231], v[78:81], v[224:227]
	ds_read_b128 v[228:231], v214 offset:4096
	v_cndmask_b32_e32 v134, v145, v223, vcc
	v_cmp_ge_u32_e32 vcc, s33, v199
	s_waitcnt lgkmcnt(1)
	v_mfma_f32_16x16x32_bf16 v[78:81], v[94:97], v[78:81], v[90:93]
	v_cndmask_b32_e32 v144, v145, v245, vcc
	v_cmp_ge_u32_e32 vcc, s33, v200
	v_mfma_f32_16x16x32_bf16 v[224:227], v[234:237], v[70:73], v[224:227]
	s_nop 0
	v_cndmask_b32_e32 v90, v145, v246, vcc
	v_cmp_ge_u32_e32 vcc, s33, v201
	s_waitcnt lgkmcnt(0)
	v_mfma_f32_16x16x32_bf16 v[70:73], v[228:231], v[70:73], v[78:81]
	v_cndmask_b32_e32 v91, v145, v247, vcc
	s_nop 1
	v_add_f32_e32 v92, v133, v227
	v_add_f32_e32 v78, v98, v224
	v_add_f32_e32 v79, v99, v225
	v_max3_f32 v80, v78, s25, v79
	v_add_f32_e32 v81, v132, v226
	v_max3_f32 v80, v80, v81, v92
	v_add_f32_e32 v70, v134, v70
	v_add_f32_e32 v71, v144, v71
	v_max3_f32 v80, v80, v70, v71
	v_add_f32_e32 v72, v90, v72
	v_add_f32_e32 v73, v91, v73
	v_max3_f32 v80, v80, v72, v73
	v_mov_b32_e32 v90, v80
	s_nop 1
	v_permlane16_swap_b32_e32 v80, v90
	v_max_f32_e32 v90, v90, v90
	v_max_f32_e32 v80, v80, v80
	v_max_f32_e32 v80, v80, v90
	v_mov_b32_e32 v90, v80
	s_nop 1
	v_permlane32_swap_b32_e32 v80, v90
	v_max3_f32 v80, v233, v80, v90
	v_sub_f32_e32 v78, v78, v80
	v_mul_f32_e32 v78, 0x3fb8aa3b, v78
	v_sub_f32_e32 v79, v79, v80
	v_sub_f32_e32 v70, v70, v80
	v_exp_f32_e32 v78, v78
	v_mul_f32_e32 v79, 0x3fb8aa3b, v79
	v_sub_f32_e32 v81, v81, v80
	v_mul_f32_e32 v70, 0x3fb8aa3b, v70
	v_exp_f32_e32 v79, v79
	v_mul_f32_e32 v81, 0x3fb8aa3b, v81
	v_sub_f32_e32 v91, v92, v80
	v_exp_f32_e32 v93, v70
	v_sub_f32_e32 v70, v71, v80
	v_exp_f32_e32 v81, v81
	v_mul_f32_e32 v91, 0x3fb8aa3b, v91
	v_mul_f32_e32 v70, 0x3fb8aa3b, v70
	v_exp_f32_e32 v91, v91
	v_exp_f32_e32 v94, v70
	v_sub_f32_e32 v70, v72, v80
	v_add_f32_e32 v92, 0, v78
	v_mul_f32_e32 v70, 0x3fb8aa3b, v70
	v_add_f32_e32 v92, v79, v92
	v_exp_f32_e32 v95, v70
	v_sub_f32_e32 v70, v73, v80
	v_add_f32_e32 v92, v81, v92
	v_mul_f32_e32 v70, 0x3fb8aa3b, v70
	v_add_f32_e32 v92, v91, v92
	v_exp_f32_e32 v73, v70
	v_add_f32_e32 v70, v93, v92
	v_add_f32_e32 v70, v94, v70
	v_sub_f32_e32 v90, v233, v80
	v_add_f32_e32 v70, v95, v70
	v_mul_f32_e32 v90, 0x3fb8aa3b, v90
	v_add_f32_e32 v92, v73, v70
	v_exp_f32_e32 v132, v90
	v_mov_b32_e32 v90, v92
	v_cvt_pk_bf16_f32 v70, v78, v79
	v_cvt_pk_bf16_f32 v71, v81, v91
	v_cvt_pk_bf16_f32 v72, v93, v94
	v_cvt_pk_bf16_f32 v73, v95, v73
	ds_read_b64_tr_b16 v[78:79], v215
	ds_read_b64_tr_b16 v[80:81], v215 offset:4096
	v_permlane16_swap_b32_e32 v92, v90
	ds_read_b64_tr_b16 v[94:95], v216
	ds_read_b64_tr_b16 v[96:97], v216 offset:4096
	v_add_f32_e32 v133, v92, v90
	v_mov_b32_e32 v134, v133
	v_mul_f32_e32 v92, v102, v132
	v_mul_f32_e32 v93, v103, v132
	v_mul_f32_e32 v90, v100, v132
	v_mul_f32_e32 v91, v101, v132
	v_permlane32_swap_b32_e32 v133, v134
	s_waitcnt lgkmcnt(2)
	v_mfma_f32_16x16x32_bf16 v[78:81], v[78:81], v[70:73], v[90:93]
	s_nop 2
	ds_read_b64_tr_b16 v[90:91], v217
	ds_read_b64_tr_b16 v[92:93], v217 offset:4096
	v_mul_f32_e32 v100, v106, v132
	v_mul_f32_e32 v101, v107, v132
	v_mul_f32_e32 v98, v104, v132
	v_mul_f32_e32 v99, v105, v132
	v_mul_f32_e32 v104, v110, v132
	v_mul_f32_e32 v105, v111, v132
	v_mul_f32_e32 v102, v108, v132
	v_mul_f32_e32 v103, v109, v132
	s_waitcnt lgkmcnt(2)
	v_mfma_f32_16x16x32_bf16 v[94:97], v[94:97], v[70:73], v[98:101]
	s_nop 2
	ds_read_b64_tr_b16 v[98:99], v218
	ds_read_b64_tr_b16 v[100:101], v218 offset:4096
	v_add_f32_e32 v133, v133, v134
	v_mul_f32_e32 v108, v114, v132
	v_mul_f32_e32 v109, v115, v132
	s_waitcnt lgkmcnt(2)
	v_mfma_f32_16x16x32_bf16 v[90:93], v[90:93], v[70:73], v[102:105]
	s_nop 2
	ds_read_b64_tr_b16 v[102:103], v219
	ds_read_b64_tr_b16 v[104:105], v219 offset:4096
	v_mul_f32_e32 v106, v112, v132
	v_mul_f32_e32 v107, v113, v132
	v_mul_f32_e32 v112, v118, v132
	v_mul_f32_e32 v113, v119, v132
	v_mul_f32_e32 v110, v116, v132
	v_mul_f32_e32 v111, v117, v132
	s_waitcnt lgkmcnt(2)
	v_mfma_f32_16x16x32_bf16 v[98:101], v[98:101], v[70:73], v[106:109]
	s_nop 2
	ds_read_b64_tr_b16 v[106:107], v220
	ds_read_b64_tr_b16 v[108:109], v220 offset:4096
	v_fmac_f32_e32 v133, v248, v132
	v_mul_f32_e32 v116, v122, v132
	v_mul_f32_e32 v117, v123, v132
	s_waitcnt lgkmcnt(2)
	v_mfma_f32_16x16x32_bf16 v[102:105], v[102:105], v[70:73], v[110:113]
	s_nop 2
	ds_read_b64_tr_b16 v[110:111], v221
	ds_read_b64_tr_b16 v[112:113], v221 offset:4096
	v_mul_f32_e32 v114, v120, v132
	v_mul_f32_e32 v115, v121, v132
	v_div_scale_f32 v122, s[34:35], v133, v133, s26
	s_waitcnt lgkmcnt(2)
	v_mfma_f32_16x16x32_bf16 v[106:109], v[106:109], v[70:73], v[114:117]
	s_nop 2
	ds_read_b64_tr_b16 v[114:115], v222
	ds_read_b64_tr_b16 v[116:117], v222 offset:4096
	v_rcp_f32_e32 v123, v122
	v_mul_f32_e32 v120, v126, v132
	v_mul_f32_e32 v121, v127, v132
	v_mul_f32_e32 v118, v124, v132
	v_mul_f32_e32 v119, v125, v132
	s_waitcnt lgkmcnt(2)
	s_nop 0
	v_mfma_f32_16x16x32_bf16 v[110:113], v[110:113], v[70:73], v[118:121]
	s_nop 2
	v_mul_f32_e64 v120, v130, v132
	v_mul_f32_e64 v121, v131, v132
	v_mul_f32_e32 v118, v128, v132
	v_mul_f32_e32 v119, v129, v132
	s_waitcnt lgkmcnt(0)
	s_nop 0
	v_mfma_f32_16x16x32_bf16 v[70:73], v[114:117], v[70:73], v[118:121]
	v_fma_f32 v114, -v122, v123, 1.0
	v_fmac_f32_e32 v123, v114, v123
	v_div_scale_f32 v114, vcc, s26, v133, s26
	v_mul_f32_e32 v115, v114, v123
	v_fma_f32 v116, -v122, v115, v114
	v_fmac_f32_e32 v115, v116, v123
	v_fma_f32 v114, -v122, v115, v114
	v_div_fmas_f32 v114, v114, v123, v115
	v_div_fixup_f32 v114, v114, v133, s26
	v_mul_f32_e32 v115, v114, v78
	v_mul_f32_e32 v79, v114, v79
	v_mov_b32_e32 v78, 0
	v_cvt_pk_fp8_f32 v78, v115, v79
	v_mul_f32_e32 v94, v114, v94
	v_mul_f32_e32 v95, v114, v95
	v_mov_b32_e32 v79, 0
	v_cvt_pk_fp8_f32 v79, v94, v95
	v_mul_f32_e32 v80, v114, v80
	v_mul_f32_e32 v81, v114, v81
	v_cvt_pk_fp8_f32 v78, v80, v81 op_sel:[0,0,1]
	v_mul_f32_e32 v80, v114, v96
	v_mul_f32_e32 v81, v114, v97
	v_cvt_pk_fp8_f32 v79, v80, v81 op_sel:[0,0,1]
	v_mul_f32_e32 v81, v114, v90
	v_mul_f32_e32 v90, v114, v91
	v_mov_b32_e32 v80, 0
	v_cvt_pk_fp8_f32 v80, v81, v90
	v_mul_f32_e32 v90, v114, v92
	v_mul_f32_e32 v91, v114, v93
	v_mul_f32_e32 v92, v114, v98
	v_mul_f32_e32 v93, v114, v99
	v_mov_b32_e32 v81, 0
	v_cvt_pk_fp8_f32 v81, v92, v93
	v_cvt_pk_fp8_f32 v80, v90, v91 op_sel:[0,0,1]
	v_mul_f32_e32 v90, v114, v100
	v_mul_f32_e32 v91, v114, v101
	v_cvt_pk_fp8_f32 v81, v90, v91 op_sel:[0,0,1]
	v_mul_f32_e32 v91, v114, v102
	v_mul_f32_e32 v92, v114, v103
	v_mov_b32_e32 v90, 0
	v_cvt_pk_fp8_f32 v90, v91, v92
	v_mul_f32_e32 v94, v114, v106
	v_mul_f32_e32 v95, v114, v107
	v_mov_b32_e32 v91, 0
	v_cvt_pk_fp8_f32 v91, v94, v95
	v_mul_f32_e32 v92, v114, v104
	v_mul_f32_e32 v93, v114, v105
	v_cvt_pk_fp8_f32 v90, v92, v93 op_sel:[0,0,1]
	v_mul_f32_e32 v92, v114, v108
	v_mul_f32_e32 v93, v114, v109
	v_cvt_pk_fp8_f32 v91, v92, v93 op_sel:[0,0,1]
	v_mul_f32_e32 v93, v114, v110
	v_mul_f32_e32 v94, v114, v111
	v_mov_b32_e32 v92, 0
	v_cvt_pk_fp8_f32 v92, v93, v94
	v_mul_f32_e32 v70, v114, v70
	v_mul_f32_e32 v71, v114, v71
	v_mov_b32_e32 v93, 0
	v_cvt_pk_fp8_f32 v93, v70, v71
	v_mul_f32_e32 v94, v114, v112
	v_mul_f32_e32 v95, v114, v113
	v_mul_f32_e32 v70, v114, v72
	v_mul_f32_e32 v71, v114, v73
	v_cvt_pk_fp8_f32 v92, v94, v95 op_sel:[0,0,1]
	v_cvt_pk_fp8_f32 v93, v70, v71 op_sel:[0,0,1]
	v_mov_b32_e32 v70, 0xc00
	v_mad_i64_i32 v[70:71], s[34:35], s29, v70, v[142:143]
	global_store_dwordx4 v[70:71], v[78:81], off
	global_store_dwordx4 v[70:71], v[90:93], off offset:16
	s_add_i32 s29, s29, s16
	v_mov_b64_e32 v[70:71], v[74:75]
	v_mov_b64_e32 v[80:81], v[68:69]
	v_mov_b64_e32 v[92:93], v[64:65]
	v_mov_b64_e32 v[96:97], v[60:61]
	s_cmp_lg_u32 s17, s30
	v_mov_b64_e32 v[72:73], v[76:77]
	v_mov_b64_e32 v[78:79], v[66:67]
	v_mov_b64_e32 v[90:91], v[62:63]
	v_mov_b64_e32 v[94:95], v[58:59]
	s_mov_b32 s34, s30
	s_cbranch_scc0 .LBB0_1965

.LBB0_1978:
	s_nop 1
	ds_read_b64 v[100:101], v223 offset:64
	v_or_b32_e32 v134, 32, v153
	v_cmp_ge_u32_e32 vcc, s33, v134
	v_or_b32_e32 v134, 33, v153
	v_or_b32_e32 v146, 34, v153
	s_waitcnt lgkmcnt(0)
	v_sub_u32_sdwa v99, s31, v100 dst_sel:DWORD dst_unused:UNUSED_PAD src0_sel:DWORD src1_sel:WORD_0
	v_med3_i32 v99, v99, 0, v1
	v_sub_u32_sdwa v100, s31, v100 dst_sel:DWORD dst_unused:UNUSED_PAD src0_sel:DWORD src1_sel:WORD_1
	v_lshl_add_u32 v99, v99, 6, v154
	v_med3_i32 v100, v100, 0, v1
	ds_read_b32 v99, v99
	v_lshl_add_u32 v100, v100, 6, v154
	s_waitcnt lgkmcnt(0)
	ds_read_b32 v100, v100
	v_cndmask_b32_e32 v99, v145, v99, vcc
	s_waitcnt lgkmcnt(0)
	v_cmp_ge_u32_e32 vcc, s33, v134
	v_or_b32_e32 v226, 48, v153
	s_add_i32 s35, s28, -5
	v_cndmask_b32_e32 v134, v145, v100, vcc
	v_sub_u32_sdwa v100, s31, v101 dst_sel:DWORD dst_unused:UNUSED_PAD src0_sel:DWORD src1_sel:WORD_0
	v_med3_i32 v100, v100, 0, v1
	v_lshl_add_u32 v100, v100, 6, v154
	ds_read_b32 v100, v100
	s_waitcnt lgkmcnt(0)
	v_cmp_ge_u32_e32 vcc, s33, v146
	s_cmp_ge_i32 s35, s27
	s_nop 0
	v_cndmask_b32_e32 v146, v145, v100, vcc
	v_sub_u32_sdwa v100, s31, v101 dst_sel:DWORD dst_unused:UNUSED_PAD src0_sel:DWORD src1_sel:WORD_1
	v_med3_i32 v100, v100, 0, v1
	v_lshl_add_u32 v100, v100, 6, v154
	ds_read_b32 v100, v100
	v_or_b32_e32 v101, 35, v153
	s_waitcnt lgkmcnt(0)
	v_cmp_ge_u32_e32 vcc, s33, v101
	s_nop 1
	v_cndmask_b32_e32 v150, v145, v100, vcc
	ds_read_b64 v[100:101], v223 offset:96
	v_cmp_ge_u32_e32 vcc, s33, v226
	v_or_b32_e32 v226, 49, v153
	s_waitcnt lgkmcnt(0)
	v_sub_u32_sdwa v152, s31, v100 dst_sel:DWORD dst_unused:UNUSED_PAD src0_sel:DWORD src1_sel:WORD_0
	v_med3_i32 v152, v152, 0, v1
	v_lshl_add_u32 v152, v152, 6, v154
	ds_read_b32 v152, v152
	s_waitcnt lgkmcnt(0)
	v_sub_u32_sdwa v100, s31, v100 dst_sel:DWORD dst_unused:UNUSED_PAD src0_sel:DWORD src1_sel:WORD_1
	v_cndmask_b32_e32 v152, v145, v152, vcc
	v_med3_i32 v100, v100, 0, v1
	v_cmp_ge_u32_e32 vcc, s33, v226
	v_sub_u32_sdwa v226, s31, v101 dst_sel:DWORD dst_unused:UNUSED_PAD src0_sel:DWORD src1_sel:WORD_0
	v_lshl_add_u32 v100, v100, 6, v154
	v_med3_i32 v226, v226, 0, v1
	v_sub_u32_sdwa v101, s31, v101 dst_sel:DWORD dst_unused:UNUSED_PAD src0_sel:DWORD src1_sel:WORD_1
	ds_read_b32 v100, v100
	v_lshl_add_u32 v226, v226, 6, v154
	v_med3_i32 v101, v101, 0, v1
	s_waitcnt lgkmcnt(0)
	ds_read_b32 v226, v226
	v_lshl_add_u32 v101, v101, 6, v154
	v_cndmask_b32_e32 v100, v145, v100, vcc
	s_waitcnt lgkmcnt(0)
	v_cmp_ge_u32_e32 vcc, s33, v155
	ds_read_b32 v101, v101
	s_waitcnt lgkmcnt(0)
	ds_read_b128 v[230:233], v212
	v_cndmask_b32_e32 v238, v145, v226, vcc
	ds_read_b128 v[226:229], v211
	s_waitcnt lgkmcnt(0)
	v_mfma_f32_16x16x32_bf16 v[226:229], v[226:229], v[94:97], 0
	ds_read_b128 v[234:237], v212 offset:4096
	v_cmp_ge_u32_e32 vcc, s33, v156
	v_mfma_f32_16x16x32_bf16 v[226:229], v[230:233], v[90:93], v[226:229]
	ds_read_b128 v[230:233], v213
	v_cndmask_b32_e32 v101, v145, v101, vcc
	s_waitcnt lgkmcnt(0)
	v_mfma_f32_16x16x32_bf16 v[226:229], v[230:233], v[78:81], v[226:229]
	ds_read_b128 v[230:233], v214
	s_waitcnt lgkmcnt(0)
	v_mfma_f32_16x16x32_bf16 v[226:229], v[230:233], v[70:73], v[226:229]
	ds_read_b128 v[230:233], v211 offset:4096
	s_nop 6
	v_add_f32_e32 v99, v99, v226
	s_waitcnt lgkmcnt(0)
	v_mfma_f32_16x16x32_bf16 v[230:233], v[230:233], v[94:97], 0
	v_add_f32_e32 v134, v134, v227
	v_max3_f32 v226, v99, s25, v134
	v_add_f32_e32 v146, v146, v228
	v_mfma_f32_16x16x32_bf16 v[230:233], v[234:237], v[90:93], v[230:233]
	ds_read_b128 v[234:237], v213 offset:4096
	v_add_f32_e32 v227, v150, v229
	v_max3_f32 v150, v226, v146, v227
	s_waitcnt lgkmcnt(0)
	v_mfma_f32_16x16x32_bf16 v[230:233], v[234:237], v[78:81], v[230:233]
	ds_read_b128 v[234:237], v214 offset:4096
	s_waitcnt lgkmcnt(0)
	v_mfma_f32_16x16x32_bf16 v[230:233], v[234:237], v[70:73], v[230:233]
	s_nop 7
	v_add_f32_e32 v152, v152, v230
	v_add_f32_e32 v100, v100, v231
	v_max3_f32 v150, v150, v152, v100
	v_add_f32_e32 v226, v238, v232
	v_add_f32_e32 v101, v101, v233
	v_max3_f32 v150, v150, v226, v101
	v_mov_b32_e32 v228, v150
	s_nop 1
	v_permlane16_swap_b32_e32 v150, v228
	v_max_f32_e32 v228, v228, v228
	v_max_f32_e32 v150, v150, v150
	v_max_f32_e32 v150, v150, v228
	v_mov_b32_e32 v228, v150
	s_nop 1
	v_permlane32_swap_b32_e32 v150, v228
	v_max3_f32 v150, v144, v150, v228
	v_sub_f32_e32 v99, v99, v150
	v_mul_f32_e32 v99, 0x3fb8aa3b, v99
	v_sub_f32_e32 v134, v134, v150
	v_exp_f32_e32 v228, v99
	v_mul_f32_e32 v134, 0x3fb8aa3b, v134
	v_sub_f32_e32 v146, v146, v150
	v_exp_f32_e32 v134, v134
	v_mul_f32_e32 v146, 0x3fb8aa3b, v146
	v_sub_f32_e32 v227, v227, v150
	v_exp_f32_e32 v146, v146
	v_mul_f32_e32 v227, 0x3fb8aa3b, v227
	v_sub_f32_e32 v152, v152, v150
	v_exp_f32_e32 v227, v227
	v_mul_f32_e32 v152, 0x3fb8aa3b, v152
	v_sub_f32_e32 v100, v100, v150
	v_add_f32_e32 v99, 0, v228
	v_exp_f32_e32 v152, v152
	v_mul_f32_e32 v100, 0x3fb8aa3b, v100
	v_sub_f32_e32 v226, v226, v150
	v_add_f32_e32 v99, v134, v99
	v_exp_f32_e32 v100, v100
	v_mul_f32_e32 v226, 0x3fb8aa3b, v226
	v_add_f32_e32 v99, v146, v99
	v_exp_f32_e32 v231, v226
	v_add_f32_e32 v99, v227, v99
	v_sub_f32_e32 v144, v144, v150
	v_add_f32_e32 v99, v152, v99
	v_sub_f32_e32 v101, v101, v150
	v_mul_f32_e32 v144, 0x3fb8aa3b, v144
	v_add_f32_e32 v99, v100, v99
	v_mul_f32_e32 v101, 0x3fb8aa3b, v101
	v_add_f32_e32 v99, v231, v99
	v_exp_f32_e32 v101, v101
	v_exp_f32_e32 v144, v144
	v_cvt_pk_bf16_f32 v228, v228, v134
	v_cvt_pk_bf16_f32 v229, v146, v227
	v_cvt_pk_bf16_f32 v230, v152, v100
	v_cvt_pk_bf16_f32 v231, v231, v101
	ds_read_b64_tr_b16 v[232:233], v215
	ds_read_b64_tr_b16 v[234:235], v215 offset:4096
	v_mul_f32_e32 v104, v104, v144
	v_mul_f32_e32 v105, v105, v144
	v_mul_f32_e32 v102, v102, v144
	v_mul_f32_e32 v103, v103, v144
	v_add_f32_e32 v99, v101, v99
	v_mul_f32_e32 v108, v108, v144
	v_mul_f32_e32 v109, v109, v144
	s_waitcnt lgkmcnt(0)
	v_mfma_f32_16x16x32_bf16 v[100:103], v[232:235], v[228:231], v[102:105]
	ds_read_b64_tr_b16 v[232:233], v216
	ds_read_b64_tr_b16 v[234:235], v216 offset:4096
	v_mul_f32_e32 v106, v106, v144
	v_mul_f32_e32 v107, v107, v144
	v_mul_f32_e32 v112, v112, v144
	v_mul_f32_e32 v113, v113, v144
	v_mul_f32_e32 v110, v110, v144
	v_mul_f32_e32 v111, v111, v144
	s_waitcnt lgkmcnt(0)
	v_mfma_f32_16x16x32_bf16 v[104:107], v[232:235], v[228:231], v[106:109]
	ds_read_b64_tr_b16 v[232:233], v217
	ds_read_b64_tr_b16 v[234:235], v217 offset:4096
	v_mul_f32_e32 v116, v116, v144
	v_mul_f32_e32 v117, v117, v144
	v_mul_f32_e32 v114, v114, v144
	v_mul_f32_e32 v115, v115, v144
	s_waitcnt lgkmcnt(0)
	v_mfma_f32_16x16x32_bf16 v[108:111], v[232:235], v[228:231], v[110:113]
	ds_read_b64_tr_b16 v[232:233], v218
	ds_read_b64_tr_b16 v[234:235], v218 offset:4096
	v_mul_f32_e32 v120, v120, v144
	v_mul_f32_e32 v121, v121, v144
	v_mul_f32_e32 v118, v118, v144
	v_mul_f32_e32 v119, v119, v144
	s_waitcnt lgkmcnt(0)
	v_mfma_f32_16x16x32_bf16 v[112:115], v[232:235], v[228:231], v[114:117]
	ds_read_b64_tr_b16 v[232:233], v219
	ds_read_b64_tr_b16 v[234:235], v219 offset:4096
	v_mul_f32_e32 v124, v124, v144
	v_mul_f32_e32 v125, v125, v144
	v_mul_f32_e32 v122, v122, v144
	v_mul_f32_e32 v123, v123, v144
	s_waitcnt lgkmcnt(0)
	v_mfma_f32_16x16x32_bf16 v[116:119], v[232:235], v[228:231], v[118:121]
	ds_read_b64_tr_b16 v[232:233], v220
	ds_read_b64_tr_b16 v[234:235], v220 offset:4096
	v_mul_f32_e32 v128, v128, v144
	v_mul_f32_e32 v129, v129, v144
	v_mul_f32_e32 v126, v126, v144
	v_mul_f32_e32 v127, v127, v144
	s_waitcnt lgkmcnt(0)
	v_mfma_f32_16x16x32_bf16 v[120:123], v[232:235], v[228:231], v[122:125]
	ds_read_b64_tr_b16 v[232:233], v221
	ds_read_b64_tr_b16 v[234:235], v221 offset:4096
	v_mov_b32_e32 v226, v99
	v_mul_f32_e32 v132, v132, v144
	v_mul_f32_e32 v133, v133, v144
	s_waitcnt lgkmcnt(0)
	v_mfma_f32_16x16x32_bf16 v[124:127], v[232:235], v[228:231], v[126:129]
	ds_read_b64_tr_b16 v[232:233], v222
	ds_read_b64_tr_b16 v[234:235], v222 offset:4096
	v_mul_f32_e32 v130, v130, v144
	v_mul_f32_e32 v131, v131, v144
	v_permlane16_swap_b32_e32 v99, v226
	s_waitcnt lgkmcnt(0)
	v_mfma_f32_16x16x32_bf16 v[128:131], v[232:235], v[228:231], v[130:133]
	v_add_f32_e32 v99, v99, v226
	v_mov_b32_e32 v226, v99
	s_nop 1
	v_permlane32_swap_b32_e32 v99, v226
	ds_write_b128 v203, v[2:5]
	ds_write_b128 v204, v[6:9]
	ds_write_b128 v205, v[18:21]
	s_waitcnt vmcnt(4)
	ds_write_b128 v206, v[22:25]
	s_waitcnt vmcnt(3)
	ds_write_b128 v207, v[34:37]
	s_waitcnt vmcnt(2)
	ds_write_b128 v208, v[38:41]
	s_waitcnt vmcnt(1)
	ds_write_b128 v209, v[50:53]
	s_waitcnt vmcnt(0)
	ds_write_b128 v210, v[54:57]
	s_cbranch_scc1 .LBB0_1980
	s_and_b32 s35, s34, 0x1fffffff
	s_mul_i32 s35, s35, s16
	s_add_i32 s35, s35, s14
	s_ashr_i32 s36, s35, 13
	s_ashr_i32 s37, s36, 31
	s_and_b32 s35, s15, 0x100
	s_lshl_b64 s[36:37], s[36:37], 21
	v_lshl_add_u32 v2, s35, 1, v151
	v_lshl_add_u64 v[50:51], v[140:141], 0, s[36:37]
	ds_read_u16 v3, v2 offset:256
	ds_read_u16 v4, v2 offset:264
	ds_read_u16 v18, v2 offset:272
	ds_read_u16 v20, v2 offset:280
	ds_read_u16 v34, v2 offset:288
	ds_read_u16 v36, v2 offset:296
	ds_read_u16 v52, v2 offset:304
	ds_read_u16 v54, v2 offset:312
	s_waitcnt lgkmcnt(7)
	v_lshlrev_b32_e32 v134, 8, v3
	v_lshl_add_u64 v[2:3], v[50:51], 0, v[134:135]
	s_waitcnt lgkmcnt(6)
	v_lshlrev_b32_e32 v134, 8, v4
	v_lshl_add_u64 v[6:7], v[50:51], 0, v[134:135]
	s_waitcnt lgkmcnt(5)
	v_lshlrev_b32_e32 v134, 8, v18
	v_lshl_add_u64 v[18:19], v[50:51], 0, v[134:135]
	s_waitcnt lgkmcnt(4)
	v_lshlrev_b32_e32 v134, 8, v20
	v_lshl_add_u64 v[22:23], v[50:51], 0, v[134:135]
	s_waitcnt lgkmcnt(3)
	v_lshlrev_b32_e32 v134, 8, v34
	v_lshl_add_u64 v[34:35], v[50:51], 0, v[134:135]
	s_waitcnt lgkmcnt(2)
	v_lshlrev_b32_e32 v134, 8, v36
	v_lshl_add_u64 v[38:39], v[50:51], 0, v[134:135]
	s_waitcnt lgkmcnt(1)
	v_lshlrev_b32_e32 v134, 8, v52
	v_lshl_add_u64 v[52:53], v[50:51], 0, v[134:135]
	s_waitcnt lgkmcnt(0)
	v_lshlrev_b32_e32 v134, 8, v54
	v_lshl_add_u64 v[54:55], v[50:51], 0, v[134:135]
	global_load_dwordx4 v[2:5], v[2:3], off
	s_nop 0
	global_load_dwordx4 v[6:9], v[6:7], off
	s_nop 0
	global_load_dwordx4 v[18:21], v[18:19], off
	s_nop 0
	global_load_dwordx4 v[22:25], v[22:23], off
	s_nop 0
	global_load_dwordx4 v[34:37], v[34:35], off
	s_nop 0
	global_load_dwordx4 v[38:41], v[38:39], off
	s_nop 0
	global_load_dwordx4 v[50:53], v[52:53], off
	s_nop 0
	global_load_dwordx4 v[54:57], v[54:55], off
.LBB0_1980:
	ds_read_b64 v[132:133], v223 offset:128
	v_cmp_ge_u32_e32 vcc, s33, v157
	s_add_i32 s35, s28, -4
	s_cmp_ge_i32 s35, s27
	s_waitcnt lgkmcnt(0)
	v_sub_u32_sdwa v134, s31, v132 dst_sel:DWORD dst_unused:UNUSED_PAD src0_sel:DWORD src1_sel:WORD_0
	v_med3_i32 v134, v134, 0, v1
	v_sub_u32_sdwa v132, s31, v132 dst_sel:DWORD dst_unused:UNUSED_PAD src0_sel:DWORD src1_sel:WORD_1
	v_lshl_add_u32 v134, v134, 6, v154
	v_med3_i32 v132, v132, 0, v1
	ds_read_b32 v134, v134
	v_lshl_add_u32 v132, v132, 6, v154
	s_waitcnt lgkmcnt(0)
	ds_read_b32 v132, v132
	v_cndmask_b32_e32 v134, v145, v134, vcc
	s_waitcnt lgkmcnt(0)
	v_cmp_gt_u32_e32 vcc, s33, v157
	s_nop 1
	v_cndmask_b32_e32 v146, v145, v132, vcc
	v_sub_u32_sdwa v132, s31, v133 dst_sel:DWORD dst_unused:UNUSED_PAD src0_sel:DWORD src1_sel:WORD_0
	v_med3_i32 v132, v132, 0, v1
	v_lshl_add_u32 v132, v132, 6, v154
	ds_read_b32 v132, v132
	s_waitcnt lgkmcnt(0)
	v_cmp_ge_u32_e32 vcc, s33, v158
	s_nop 1
	v_cndmask_b32_e32 v152, v145, v132, vcc
	v_sub_u32_sdwa v132, s31, v133 dst_sel:DWORD dst_unused:UNUSED_PAD src0_sel:DWORD src1_sel:WORD_1
	v_med3_i32 v132, v132, 0, v1
	v_lshl_add_u32 v132, v132, 6, v154
	ds_read_b32 v132, v132
	s_waitcnt lgkmcnt(0)
	v_cmp_ge_u32_e32 vcc, s33, v159
	s_nop 1
	v_cndmask_b32_e32 v227, v145, v132, vcc
	ds_read_b64 v[132:133], v223 offset:160
	v_cmp_ge_u32_e32 vcc, s33, v160
	s_waitcnt lgkmcnt(0)
	v_sub_u32_sdwa v228, s31, v132 dst_sel:DWORD dst_unused:UNUSED_PAD src0_sel:DWORD src1_sel:WORD_0
	v_med3_i32 v228, v228, 0, v1
	v_lshl_add_u32 v228, v228, 6, v154
	ds_read_b32 v228, v228
	s_waitcnt lgkmcnt(0)
	v_sub_u32_sdwa v132, s31, v132 dst_sel:DWORD dst_unused:UNUSED_PAD src0_sel:DWORD src1_sel:WORD_1
	v_cndmask_b32_e32 v240, v145, v228, vcc
	v_med3_i32 v132, v132, 0, v1
	v_sub_u32_sdwa v228, s31, v133 dst_sel:DWORD dst_unused:UNUSED_PAD src0_sel:DWORD src1_sel:WORD_0
	v_lshl_add_u32 v132, v132, 6, v154
	v_med3_i32 v228, v228, 0, v1
	v_sub_u32_sdwa v133, s31, v133 dst_sel:DWORD dst_unused:UNUSED_PAD src0_sel:DWORD src1_sel:WORD_1
	ds_read_b32 v132, v132
	v_lshl_add_u32 v228, v228, 6, v154
	v_med3_i32 v133, v133, 0, v1
	s_waitcnt lgkmcnt(0)
	v_cmp_ge_u32_e32 vcc, s33, v161
	ds_read_b32 v228, v228
	v_lshl_add_u32 v133, v133, 6, v154
	v_cndmask_b32_e32 v132, v145, v132, vcc
	s_waitcnt lgkmcnt(0)
	v_cmp_ge_u32_e32 vcc, s33, v162
	ds_read_b32 v133, v133
	s_waitcnt lgkmcnt(0)
	ds_read_b128 v[232:235], v212
	v_cndmask_b32_e32 v241, v145, v228, vcc
	ds_read_b128 v[228:231], v211
	s_waitcnt lgkmcnt(0)
	v_mfma_f32_16x16x32_bf16 v[228:231], v[228:231], v[94:97], 0
	ds_read_b128 v[236:239], v212 offset:4096
	v_cmp_ge_u32_e32 vcc, s33, v163
	v_mfma_f32_16x16x32_bf16 v[228:231], v[232:235], v[90:93], v[228:231]
	ds_read_b128 v[232:235], v213
	v_cndmask_b32_e32 v133, v145, v133, vcc
	s_waitcnt lgkmcnt(0)
	v_mfma_f32_16x16x32_bf16 v[228:231], v[232:235], v[78:81], v[228:231]
	ds_read_b128 v[232:235], v214
	s_waitcnt lgkmcnt(0)
	v_mfma_f32_16x16x32_bf16 v[228:231], v[232:235], v[70:73], v[228:231]
	ds_read_b128 v[232:235], v211 offset:4096
	s_nop 6
	v_add_f32_e32 v134, v134, v228
	s_waitcnt lgkmcnt(0)
	v_mfma_f32_16x16x32_bf16 v[232:235], v[232:235], v[94:97], 0
	v_add_f32_e32 v228, v146, v229
	v_max3_f32 v146, v134, s25, v228
	v_add_f32_e32 v152, v152, v230
	v_mfma_f32_16x16x32_bf16 v[232:235], v[236:239], v[90:93], v[232:235]
	ds_read_b128 v[236:239], v213 offset:4096
	v_add_f32_e32 v227, v227, v231
	v_max3_f32 v146, v146, v152, v227
	s_waitcnt lgkmcnt(0)
	v_mfma_f32_16x16x32_bf16 v[232:235], v[236:239], v[78:81], v[232:235]
	ds_read_b128 v[236:239], v214 offset:4096
	s_waitcnt lgkmcnt(0)
	v_mfma_f32_16x16x32_bf16 v[232:235], v[236:239], v[70:73], v[232:235]
	s_nop 7
	v_add_f32_e32 v229, v240, v232
	v_add_f32_e32 v132, v132, v233
	v_max3_f32 v146, v146, v229, v132
	v_add_f32_e32 v230, v241, v234
	v_add_f32_e32 v133, v133, v235
	v_max3_f32 v146, v146, v230, v133
	v_mov_b32_e32 v231, v146
	s_nop 1
	v_permlane16_swap_b32_e32 v146, v231
	v_max_f32_e32 v231, v231, v231
	v_max_f32_e32 v146, v146, v146
	v_max_f32_e32 v146, v146, v231
	v_mov_b32_e32 v231, v146
	s_nop 1
	v_permlane32_swap_b32_e32 v146, v231
	v_max3_f32 v146, v150, v146, v231
	v_sub_f32_e32 v134, v134, v146
	v_mul_f32_e32 v134, 0x3fb8aa3b, v134
	v_sub_f32_e32 v228, v228, v146
	v_exp_f32_e32 v134, v134
	v_mul_f32_e32 v228, 0x3fb8aa3b, v228
	v_sub_f32_e32 v152, v152, v146
	v_exp_f32_e32 v228, v228
	v_mul_f32_e32 v152, 0x3fb8aa3b, v152
	v_sub_f32_e32 v227, v227, v146
	v_exp_f32_e32 v152, v152
	v_mul_f32_e32 v227, 0x3fb8aa3b, v227
	v_exp_f32_e32 v232, v227
	v_add_f32_e32 v231, 0, v134
	v_add_f32_e32 v231, v228, v231
	v_sub_f32_e32 v229, v229, v146
	v_add_f32_e32 v231, v152, v231
	v_mul_f32_e32 v229, 0x3fb8aa3b, v229
	v_sub_f32_e32 v132, v132, v146
	v_add_f32_e32 v227, v232, v231
	v_exp_f32_e32 v231, v229
	v_mul_f32_e32 v132, 0x3fb8aa3b, v132
	v_exp_f32_e32 v233, v132
	v_sub_f32_e32 v133, v133, v146
	v_add_f32_e32 v227, v231, v227
	v_mul_f32_e32 v133, 0x3fb8aa3b, v133
	v_add_f32_e32 v132, v233, v227
	v_sub_f32_e32 v227, v230, v146
	v_mul_f32_e32 v227, 0x3fb8aa3b, v227
	v_exp_f32_e32 v234, v227
	v_exp_f32_e32 v235, v133
	v_sub_f32_e32 v150, v150, v146
	v_mul_f32_e32 v150, 0x3fb8aa3b, v150
	v_add_f32_e32 v132, v234, v132
	v_add_f32_e32 v133, v235, v132
	v_exp_f32_e32 v132, v150
	v_mov_b32_e32 v150, v133
	s_nop 1
	v_permlane16_swap_b32_e32 v133, v150
	v_cvt_pk_bf16_f32 v228, v134, v228
	v_cvt_pk_bf16_f32 v229, v152, v232
	v_cvt_pk_bf16_f32 v230, v231, v233
	v_cvt_pk_bf16_f32 v231, v234, v235
	ds_read_b64_tr_b16 v[232:233], v215
	ds_read_b64_tr_b16 v[234:235], v215 offset:4096
	v_add_f32_e32 v133, v133, v150
	v_mov_b32_e32 v227, v133
	s_nop 1
	v_permlane32_swap_b32_e32 v133, v227
	v_mul_f32_e32 v102, v102, v132
	v_mul_f32_e32 v103, v103, v132
	v_mul_f32_e32 v100, v100, v132
	v_mul_f32_e32 v101, v101, v132
	v_mul_f32_e32 v106, v106, v132
	v_mul_f32_e32 v107, v107, v132
	v_mul_f32_e32 v104, v104, v132
	v_mul_f32_e32 v105, v105, v132
	s_waitcnt lgkmcnt(0)
	v_mfma_f32_16x16x32_bf16 v[100:103], v[232:235], v[228:231], v[100:103]
	ds_read_b64_tr_b16 v[232:233], v216
	ds_read_b64_tr_b16 v[234:235], v216 offset:4096
	v_mul_f32_e32 v110, v110, v132
	v_mul_f32_e32 v111, v111, v132
	v_mul_f32_e32 v108, v108, v132
	v_mul_f32_e32 v109, v109, v132
	s_waitcnt lgkmcnt(0)
	v_mfma_f32_16x16x32_bf16 v[104:107], v[232:235], v[228:231], v[104:107]
	ds_read_b64_tr_b16 v[232:233], v217
	ds_read_b64_tr_b16 v[234:235], v217 offset:4096
	v_mul_f32_e32 v114, v114, v132
	v_mul_f32_e32 v115, v115, v132
	v_mul_f32_e32 v112, v112, v132
	v_mul_f32_e32 v113, v113, v132
	s_waitcnt lgkmcnt(0)
	v_mfma_f32_16x16x32_bf16 v[108:111], v[232:235], v[228:231], v[108:111]
	ds_read_b64_tr_b16 v[232:233], v218
	ds_read_b64_tr_b16 v[234:235], v218 offset:4096
	v_mul_f32_e32 v118, v118, v132
	v_mul_f32_e32 v119, v119, v132
	v_mul_f32_e32 v116, v116, v132
	v_mul_f32_e32 v117, v117, v132
	s_waitcnt lgkmcnt(0)
	v_mfma_f32_16x16x32_bf16 v[112:115], v[232:235], v[228:231], v[112:115]
	ds_read_b64_tr_b16 v[232:233], v219
	ds_read_b64_tr_b16 v[234:235], v219 offset:4096
	v_mul_f32_e32 v122, v122, v132
	v_mul_f32_e32 v123, v123, v132
	v_mul_f32_e32 v120, v120, v132
	v_mul_f32_e32 v121, v121, v132
	s_waitcnt lgkmcnt(0)
	v_mfma_f32_16x16x32_bf16 v[116:119], v[232:235], v[228:231], v[116:119]
	ds_read_b64_tr_b16 v[232:233], v220
	ds_read_b64_tr_b16 v[234:235], v220 offset:4096
	v_mul_f32_e32 v126, v126, v132
	v_mul_f32_e32 v127, v127, v132
	v_mul_f32_e32 v124, v124, v132
	v_mul_f32_e32 v125, v125, v132
	s_waitcnt lgkmcnt(0)
	v_mfma_f32_16x16x32_bf16 v[120:123], v[232:235], v[228:231], v[120:123]
	ds_read_b64_tr_b16 v[232:233], v221
	ds_read_b64_tr_b16 v[234:235], v221 offset:4096
	v_mul_f32_e32 v130, v130, v132
	v_mul_f32_e32 v131, v131, v132
	v_mul_f32_e32 v128, v128, v132
	v_mul_f32_e32 v129, v129, v132
	s_waitcnt lgkmcnt(0)
	v_mfma_f32_16x16x32_bf16 v[124:127], v[232:235], v[228:231], v[124:127]
	ds_read_b64_tr_b16 v[232:233], v222
	ds_read_b64_tr_b16 v[234:235], v222 offset:4096
	ds_write_b128 v203, v[10:13]
	ds_write_b128 v204, v[14:17]
	ds_write_b128 v205, v[26:29]
	ds_write_b128 v206, v[30:33]
	ds_write_b128 v207, v[42:45]
	ds_write_b128 v208, v[46:49]
	ds_write_b128 v209, v[82:85]
	ds_write_b128 v210, v[86:89]
	s_waitcnt lgkmcnt(8)
	v_mfma_f32_16x16x32_bf16 v[128:131], v[232:235], v[228:231], v[128:131]
	s_cbranch_scc1 .LBB0_1982
	s_and_b32 s35, s34, 0x1fffffff
	s_mul_i32 s35, s35, s16
	s_add_i32 s35, s35, s14
	s_ashr_i32 s36, s35, 13
	s_ashr_i32 s37, s36, 31
	s_and_b32 s35, s15, 0x100
	s_lshl_b64 s[36:37], s[36:37], 21
	v_lshl_add_u32 v10, s35, 1, v151
	v_lshl_add_u64 v[82:83], v[140:141], 0, s[36:37]
	ds_read_u16 v11, v10 offset:320
	ds_read_u16 v12, v10 offset:328
	ds_read_u16 v26, v10 offset:336
	ds_read_u16 v28, v10 offset:344
	ds_read_u16 v42, v10 offset:352
	ds_read_u16 v44, v10 offset:360
	ds_read_u16 v84, v10 offset:368
	ds_read_u16 v86, v10 offset:376
	s_waitcnt lgkmcnt(7)
	v_lshlrev_b32_e32 v134, 8, v11
	v_lshl_add_u64 v[10:11], v[82:83], 0, v[134:135]
	s_waitcnt lgkmcnt(6)
	v_lshlrev_b32_e32 v134, 8, v12
	v_lshl_add_u64 v[14:15], v[82:83], 0, v[134:135]
	s_waitcnt lgkmcnt(5)
	v_lshlrev_b32_e32 v134, 8, v26
	v_lshl_add_u64 v[26:27], v[82:83], 0, v[134:135]
	s_waitcnt lgkmcnt(4)
	v_lshlrev_b32_e32 v134, 8, v28
	v_lshl_add_u64 v[30:31], v[82:83], 0, v[134:135]
	s_waitcnt lgkmcnt(3)
	v_lshlrev_b32_e32 v134, 8, v42
	v_lshl_add_u64 v[42:43], v[82:83], 0, v[134:135]
	s_waitcnt lgkmcnt(2)
	v_lshlrev_b32_e32 v134, 8, v44
	v_lshl_add_u64 v[46:47], v[82:83], 0, v[134:135]
	s_waitcnt lgkmcnt(1)
	v_lshlrev_b32_e32 v134, 8, v84
	v_lshl_add_u64 v[84:85], v[82:83], 0, v[134:135]
	s_waitcnt lgkmcnt(0)
	v_lshlrev_b32_e32 v134, 8, v86
	v_lshl_add_u64 v[86:87], v[82:83], 0, v[134:135]
	global_load_dwordx4 v[10:13], v[10:11], off
	s_nop 0
	global_load_dwordx4 v[14:17], v[14:15], off
	s_nop 0
	global_load_dwordx4 v[26:29], v[26:27], off
	s_nop 0
	global_load_dwordx4 v[30:33], v[30:31], off
	s_nop 0
	global_load_dwordx4 v[42:45], v[42:43], off
	s_nop 0
	global_load_dwordx4 v[46:49], v[46:47], off
	s_nop 0
	global_load_dwordx4 v[82:85], v[84:85], off
	s_nop 0
	global_load_dwordx4 v[86:89], v[86:87], off
.LBB0_1982:
	ds_read_b64 v[228:229], v223 offset:192
	v_cmp_ge_u32_e32 vcc, s33, v164
	s_xor_b32 s4, s4, 0x200
	v_add_u32_e32 v134, s4, v147
	s_add_i32 s4, s28, -3
	s_waitcnt lgkmcnt(0)
	v_sub_u32_sdwa v150, s31, v228 dst_sel:DWORD dst_unused:UNUSED_PAD src0_sel:DWORD src1_sel:WORD_0
	v_med3_i32 v150, v150, 0, v1
	v_sub_u32_sdwa v152, s31, v228 dst_sel:DWORD dst_unused:UNUSED_PAD src0_sel:DWORD src1_sel:WORD_1
	v_lshl_add_u32 v150, v150, 6, v154
	v_med3_i32 v152, v152, 0, v1
	v_sub_u32_sdwa v228, s31, v229 dst_sel:DWORD dst_unused:UNUSED_PAD src0_sel:DWORD src1_sel:WORD_0
	ds_read_b32 v150, v150
	v_lshl_add_u32 v152, v152, 6, v154
	v_med3_i32 v228, v228, 0, v1
	s_waitcnt lgkmcnt(0)
	ds_read_b32 v152, v152
	v_lshl_add_u32 v228, v228, 6, v154
	v_cndmask_b32_e32 v150, v145, v150, vcc
	s_waitcnt lgkmcnt(0)
	v_cmp_ge_u32_e32 vcc, s33, v165
	ds_read_b32 v228, v228
	s_waitcnt lgkmcnt(0)
	s_cmp_ge_i32 s4, s27
	v_cndmask_b32_e32 v152, v145, v152, vcc
	v_cmp_ge_u32_e32 vcc, s33, v166
	s_nop 1
	v_cndmask_b32_e32 v240, v145, v228, vcc
	v_sub_u32_sdwa v228, s31, v229 dst_sel:DWORD dst_unused:UNUSED_PAD src0_sel:DWORD src1_sel:WORD_1
	v_med3_i32 v228, v228, 0, v1
	v_lshl_add_u32 v228, v228, 6, v154
	ds_read_b32 v228, v228
	s_waitcnt lgkmcnt(0)
	v_cmp_ge_u32_e32 vcc, s33, v167
	s_nop 1
	v_cndmask_b32_e32 v241, v145, v228, vcc
	ds_read_b64 v[228:229], v223 offset:224
	v_cmp_ge_u32_e32 vcc, s33, v168
	s_waitcnt lgkmcnt(0)
	v_sub_u32_sdwa v230, s31, v228 dst_sel:DWORD dst_unused:UNUSED_PAD src0_sel:DWORD src1_sel:WORD_0
	v_med3_i32 v230, v230, 0, v1
	v_sub_u32_sdwa v228, s31, v228 dst_sel:DWORD dst_unused:UNUSED_PAD src0_sel:DWORD src1_sel:WORD_1
	v_lshl_add_u32 v230, v230, 6, v154
	v_med3_i32 v228, v228, 0, v1
	ds_read_b32 v230, v230
	v_lshl_add_u32 v228, v228, 6, v154
	s_waitcnt lgkmcnt(0)
	ds_read_b32 v228, v228
	v_cndmask_b32_e32 v242, v145, v230, vcc
	s_waitcnt lgkmcnt(0)
	v_cmp_ge_u32_e32 vcc, s33, v169
	s_nop 1
	v_cndmask_b32_e32 v243, v145, v228, vcc
	v_sub_u32_sdwa v228, s31, v229 dst_sel:DWORD dst_unused:UNUSED_PAD src0_sel:DWORD src1_sel:WORD_0
	v_med3_i32 v228, v228, 0, v1
	v_lshl_add_u32 v228, v228, 6, v154
	ds_read_b32 v228, v228
	s_waitcnt lgkmcnt(0)
	v_cmp_ge_u32_e32 vcc, s33, v170
	s_nop 1
	v_cndmask_b32_e32 v244, v145, v228, vcc
	v_sub_u32_sdwa v228, s31, v229 dst_sel:DWORD dst_unused:UNUSED_PAD src0_sel:DWORD src1_sel:WORD_1
	v_med3_i32 v228, v228, 0, v1
	v_lshl_add_u32 v228, v228, 6, v154
	ds_read_b32 v228, v228
	s_waitcnt lgkmcnt(0)
	v_cmp_ge_u32_e32 vcc, s33, v171
	ds_read_b128 v[232:235], v212
	ds_read_b128 v[236:239], v212 offset:4096
	v_cndmask_b32_e32 v245, v145, v228, vcc
	ds_read_b128 v[228:231], v211
	s_waitcnt lgkmcnt(0)
	v_mfma_f32_16x16x32_bf16 v[228:231], v[228:231], v[94:97], 0
	v_mfma_f32_16x16x32_bf16 v[228:231], v[232:235], v[90:93], v[228:231]
	ds_read_b128 v[232:235], v213
	s_waitcnt lgkmcnt(0)
	v_mfma_f32_16x16x32_bf16 v[228:231], v[232:235], v[78:81], v[228:231]
	ds_read_b128 v[232:235], v214
	s_waitcnt lgkmcnt(0)
	v_mfma_f32_16x16x32_bf16 v[228:231], v[232:235], v[70:73], v[228:231]
	ds_read_b128 v[232:235], v211 offset:4096
	s_nop 6
	v_add_f32_e32 v228, v150, v228
	s_waitcnt lgkmcnt(0)
	v_mfma_f32_16x16x32_bf16 v[232:235], v[232:235], v[94:97], 0
	v_add_f32_e32 v152, v152, v229
	v_max3_f32 v150, v228, s25, v152
	v_add_f32_e32 v229, v240, v230
	v_mfma_f32_16x16x32_bf16 v[232:235], v[236:239], v[90:93], v[232:235]
	ds_read_b128 v[236:239], v213 offset:4096
	v_add_f32_e32 v230, v241, v231
	v_max3_f32 v150, v150, v229, v230
	s_waitcnt lgkmcnt(0)
	v_mfma_f32_16x16x32_bf16 v[232:235], v[236:239], v[78:81], v[232:235]
	ds_read_b128 v[236:239], v214 offset:4096
	s_waitcnt lgkmcnt(0)
	v_mfma_f32_16x16x32_bf16 v[232:235], v[236:239], v[70:73], v[232:235]
	s_nop 7
	v_add_f32_e32 v231, v242, v232
	v_add_f32_e32 v232, v243, v233
	v_max3_f32 v150, v150, v231, v232
	v_add_f32_e32 v233, v244, v234
	v_add_f32_e32 v234, v245, v235
	v_max3_f32 v150, v150, v233, v234
	v_mov_b32_e32 v235, v150
	s_nop 1
	v_permlane16_swap_b32_e32 v150, v235
	v_max_f32_e32 v235, v235, v235
	v_max_f32_e32 v150, v150, v150
	v_max_f32_e32 v150, v150, v235
	v_mov_b32_e32 v235, v150
	s_nop 1
	v_permlane32_swap_b32_e32 v150, v235
	v_max3_f32 v150, v146, v150, v235
	v_sub_f32_e32 v229, v229, v150
	v_mul_f32_e32 v229, 0x3fb8aa3b, v229
	v_exp_f32_e32 v236, v229
	v_sub_f32_e32 v229, v230, v150
	v_sub_f32_e32 v228, v228, v150
	v_mul_f32_e32 v229, 0x3fb8aa3b, v229
	v_mul_f32_e32 v228, 0x3fb8aa3b, v228
	v_sub_f32_e32 v152, v152, v150
	v_exp_f32_e32 v237, v229
	v_sub_f32_e32 v229, v231, v150
	v_exp_f32_e32 v235, v228
	v_mul_f32_e32 v152, 0x3fb8aa3b, v152
	v_mul_f32_e32 v229, 0x3fb8aa3b, v229
	v_exp_f32_e32 v152, v152
	v_exp_f32_e32 v238, v229
	v_sub_f32_e32 v229, v232, v150
	v_mul_f32_e32 v229, 0x3fb8aa3b, v229
	v_exp_f32_e32 v232, v229
	v_sub_f32_e32 v229, v233, v150
	v_add_f32_e32 v228, 0, v235
	v_mul_f32_e32 v229, 0x3fb8aa3b, v229
	v_add_f32_e32 v228, v152, v228
	v_exp_f32_e32 v233, v229
	v_sub_f32_e32 v229, v234, v150
	v_add_f32_e32 v228, v236, v228
	v_mul_f32_e32 v229, 0x3fb8aa3b, v229
	v_add_f32_e32 v228, v237, v228
	v_exp_f32_e32 v234, v229
	v_add_f32_e32 v228, v238, v228
	v_sub_f32_e32 v146, v146, v150
	v_add_f32_e32 v228, v232, v228
	v_mul_f32_e32 v146, 0x3fb8aa3b, v146
	v_add_f32_e32 v228, v233, v228
	v_add_f32_e32 v228, v234, v228
	v_exp_f32_e32 v146, v146
	v_cvt_pk_bf16_f32 v230, v235, v152
	v_cvt_pk_bf16_f32 v231, v236, v237
	v_cvt_pk_bf16_f32 v232, v238, v232
	v_cvt_pk_bf16_f32 v233, v233, v234
	ds_read_b64_tr_b16 v[234:235], v215
	ds_read_b64_tr_b16 v[236:237], v215 offset:4096
	v_mul_f32_e32 v102, v102, v146
	v_mul_f32_e32 v103, v103, v146
	v_mul_f32_e32 v100, v100, v146
	v_mul_f32_e32 v101, v101, v146
	v_mul_f32_e32 v106, v106, v146
	v_mul_f32_e32 v107, v107, v146
	v_mul_f32_e32 v104, v104, v146
	v_mul_f32_e32 v105, v105, v146
	s_waitcnt lgkmcnt(0)
	v_mfma_f32_16x16x32_bf16 v[100:103], v[234:237], v[230:233], v[100:103]
	ds_read_b64_tr_b16 v[234:235], v216
	ds_read_b64_tr_b16 v[236:237], v216 offset:4096
	v_mul_f32_e32 v110, v110, v146
	v_mul_f32_e32 v111, v111, v146
	v_mul_f32_e32 v108, v108, v146
	v_mul_f32_e32 v109, v109, v146
	s_waitcnt lgkmcnt(0)
	v_mfma_f32_16x16x32_bf16 v[104:107], v[234:237], v[230:233], v[104:107]
	ds_read_b64_tr_b16 v[234:235], v217
	ds_read_b64_tr_b16 v[236:237], v217 offset:4096
	v_mul_f32_e32 v114, v114, v146
	v_mul_f32_e32 v115, v115, v146
	v_mul_f32_e32 v112, v112, v146
	v_mul_f32_e32 v113, v113, v146
	s_waitcnt lgkmcnt(0)
	v_mfma_f32_16x16x32_bf16 v[108:111], v[234:237], v[230:233], v[108:111]
	ds_read_b64_tr_b16 v[234:235], v218
	ds_read_b64_tr_b16 v[236:237], v218 offset:4096
	v_mul_f32_e32 v118, v118, v146
	v_mul_f32_e32 v119, v119, v146
	v_mul_f32_e32 v116, v116, v146
	v_mul_f32_e32 v117, v117, v146
	s_waitcnt lgkmcnt(0)
	v_mfma_f32_16x16x32_bf16 v[112:115], v[234:237], v[230:233], v[112:115]
	ds_read_b64_tr_b16 v[234:235], v219
	ds_read_b64_tr_b16 v[236:237], v219 offset:4096
	v_mul_f32_e32 v122, v122, v146
	v_mul_f32_e32 v123, v123, v146
	v_mul_f32_e32 v120, v120, v146
	v_mul_f32_e32 v121, v121, v146
	s_waitcnt lgkmcnt(0)
	v_mfma_f32_16x16x32_bf16 v[116:119], v[234:237], v[230:233], v[116:119]
	ds_read_b64_tr_b16 v[234:235], v220
	ds_read_b64_tr_b16 v[236:237], v220 offset:4096
	v_mul_f32_e32 v126, v126, v146
	v_mul_f32_e32 v127, v127, v146
	v_mul_f32_e32 v124, v124, v146
	v_mul_f32_e32 v125, v125, v146
	s_waitcnt lgkmcnt(0)
	v_mfma_f32_16x16x32_bf16 v[120:123], v[234:237], v[230:233], v[120:123]
	ds_read_b64_tr_b16 v[234:235], v221
	ds_read_b64_tr_b16 v[236:237], v221 offset:4096
	v_mov_b32_e32 v229, v228
	v_mul_f32_e32 v130, v130, v146
	v_mul_f32_e32 v131, v131, v146
	s_waitcnt lgkmcnt(0)
	v_mfma_f32_16x16x32_bf16 v[124:127], v[234:237], v[230:233], v[124:127]
	ds_read_b64_tr_b16 v[234:235], v222
	ds_read_b64_tr_b16 v[236:237], v222 offset:4096
	v_mul_f32_e32 v128, v128, v146
	v_mul_f32_e32 v129, v129, v146
	v_permlane16_swap_b32_e32 v228, v229
	s_waitcnt lgkmcnt(0)
	v_mfma_f32_16x16x32_bf16 v[128:131], v[234:237], v[230:233], v[128:131]
	v_add_f32_e32 v228, v228, v229
	v_mov_b32_e32 v229, v228
	s_nop 1
	v_permlane32_swap_b32_e32 v228, v229
	ds_write_b64 v134, v[148:149]
	s_waitcnt vmcnt(7)
	ds_write_b128 v203, v[2:5]
	s_waitcnt vmcnt(6)
	ds_write_b128 v204, v[6:9]
	s_waitcnt vmcnt(5)
	ds_write_b128 v205, v[18:21]
	s_waitcnt vmcnt(4)
	ds_write_b128 v206, v[22:25]
	s_waitcnt vmcnt(3)
	ds_write_b128 v207, v[34:37]
	s_waitcnt vmcnt(2)
	ds_write_b128 v208, v[38:41]
	s_waitcnt vmcnt(1)
	ds_write_b128 v209, v[50:53]
	s_waitcnt vmcnt(0)
	ds_write_b128 v210, v[54:57]
	s_cbranch_scc1 .LBB0_1984
	s_and_b32 s4, s34, 0x1fffffff
	s_mul_i32 s4, s4, s16
	s_add_i32 s4, s4, s14
	s_ashr_i32 s36, s4, 13
	s_ashr_i32 s37, s36, 31
	s_and_b32 s4, s15, 0x100
	s_lshl_b64 s[36:37], s[36:37], 21
	v_lshl_add_u32 v2, s4, 1, v151
	v_lshl_add_u64 v[50:51], v[140:141], 0, s[36:37]
	ds_read_u16 v3, v2 offset:384
	ds_read_u16 v4, v2 offset:392
	ds_read_u16 v18, v2 offset:400
	ds_read_u16 v20, v2 offset:408
	ds_read_u16 v34, v2 offset:416
	ds_read_u16 v36, v2 offset:424
	ds_read_u16 v52, v2 offset:432
	ds_read_u16 v54, v2 offset:440
	s_waitcnt lgkmcnt(7)
	v_lshlrev_b32_e32 v134, 8, v3
	v_lshl_add_u64 v[2:3], v[50:51], 0, v[134:135]
	s_waitcnt lgkmcnt(6)
	v_lshlrev_b32_e32 v134, 8, v4
	v_lshl_add_u64 v[6:7], v[50:51], 0, v[134:135]
	s_waitcnt lgkmcnt(5)
	v_lshlrev_b32_e32 v134, 8, v18
	v_lshl_add_u64 v[18:19], v[50:51], 0, v[134:135]
	s_waitcnt lgkmcnt(4)
	v_lshlrev_b32_e32 v134, 8, v20
	v_lshl_add_u64 v[22:23], v[50:51], 0, v[134:135]
	s_waitcnt lgkmcnt(3)
	v_lshlrev_b32_e32 v134, 8, v34
	v_lshl_add_u64 v[34:35], v[50:51], 0, v[134:135]
	s_waitcnt lgkmcnt(2)
	v_lshlrev_b32_e32 v134, 8, v36
	v_lshl_add_u64 v[38:39], v[50:51], 0, v[134:135]
	s_waitcnt lgkmcnt(1)
	v_lshlrev_b32_e32 v134, 8, v52
	v_lshl_add_u64 v[52:53], v[50:51], 0, v[134:135]
	s_waitcnt lgkmcnt(0)
	v_lshlrev_b32_e32 v134, 8, v54
	v_lshl_add_u64 v[54:55], v[50:51], 0, v[134:135]
	global_load_dwordx4 v[2:5], v[2:3], off
	s_nop 0
	global_load_dwordx4 v[6:9], v[6:7], off
	s_nop 0
	global_load_dwordx4 v[18:21], v[18:19], off
	s_nop 0
	global_load_dwordx4 v[22:25], v[22:23], off
	s_nop 0
	global_load_dwordx4 v[34:37], v[34:35], off
	s_nop 0
	global_load_dwordx4 v[38:41], v[38:39], off
	s_nop 0
	global_load_dwordx4 v[50:53], v[52:53], off
	s_nop 0
	global_load_dwordx4 v[54:57], v[54:55], off
.LBB0_1984:
	ds_read_b64 v[148:149], v223 offset:256
	v_cmp_ge_u32_e32 vcc, s33, v172
	s_add_i32 s4, s28, -2
	s_cmp_ge_i32 s4, s27
	s_waitcnt lgkmcnt(0)
	v_sub_u32_sdwa v134, s31, v148 dst_sel:DWORD dst_unused:UNUSED_PAD src0_sel:DWORD src1_sel:WORD_0
	v_med3_i32 v134, v134, 0, v1
	v_sub_u32_sdwa v148, s31, v148 dst_sel:DWORD dst_unused:UNUSED_PAD src0_sel:DWORD src1_sel:WORD_1
	v_lshl_add_u32 v134, v134, 6, v154
	v_med3_i32 v148, v148, 0, v1
	ds_read_b32 v134, v134
	v_lshl_add_u32 v148, v148, 6, v154
	s_waitcnt lgkmcnt(0)
	ds_read_b32 v148, v148
	v_cndmask_b32_e32 v134, v145, v134, vcc
	s_waitcnt lgkmcnt(0)
	v_cmp_gt_u32_e32 vcc, s33, v172
	s_nop 1
	v_cndmask_b32_e32 v152, v145, v148, vcc
	v_sub_u32_sdwa v148, s31, v149 dst_sel:DWORD dst_unused:UNUSED_PAD src0_sel:DWORD src1_sel:WORD_0
	v_med3_i32 v148, v148, 0, v1
	v_lshl_add_u32 v148, v148, 6, v154
	ds_read_b32 v148, v148
	s_waitcnt lgkmcnt(0)
	v_cmp_ge_u32_e32 vcc, s33, v173
	s_nop 1
	v_cndmask_b32_e32 v242, v145, v148, vcc
	v_sub_u32_sdwa v148, s31, v149 dst_sel:DWORD dst_unused:UNUSED_PAD src0_sel:DWORD src1_sel:WORD_1
	v_med3_i32 v148, v148, 0, v1
	v_lshl_add_u32 v148, v148, 6, v154
	ds_read_b32 v148, v148
	s_waitcnt lgkmcnt(0)
	v_cmp_ge_u32_e32 vcc, s33, v174
	s_nop 1
	v_cndmask_b32_e32 v243, v145, v148, vcc
	ds_read_b64 v[148:149], v223 offset:288
	v_cmp_ge_u32_e32 vcc, s33, v175
	s_waitcnt lgkmcnt(0)
	v_sub_u32_sdwa v230, s31, v148 dst_sel:DWORD dst_unused:UNUSED_PAD src0_sel:DWORD src1_sel:WORD_0
	v_med3_i32 v230, v230, 0, v1
	v_lshl_add_u32 v230, v230, 6, v154
	ds_read_b32 v230, v230
	s_waitcnt lgkmcnt(0)
	v_sub_u32_sdwa v148, s31, v148 dst_sel:DWORD dst_unused:UNUSED_PAD src0_sel:DWORD src1_sel:WORD_1
	v_cndmask_b32_e32 v244, v145, v230, vcc
	v_med3_i32 v148, v148, 0, v1
	v_sub_u32_sdwa v230, s31, v149 dst_sel:DWORD dst_unused:UNUSED_PAD src0_sel:DWORD src1_sel:WORD_0
	v_lshl_add_u32 v148, v148, 6, v154
	v_med3_i32 v230, v230, 0, v1
	v_sub_u32_sdwa v149, s31, v149 dst_sel:DWORD dst_unused:UNUSED_PAD src0_sel:DWORD src1_sel:WORD_1
	ds_read_b32 v148, v148
	v_lshl_add_u32 v230, v230, 6, v154
	v_med3_i32 v149, v149, 0, v1
	s_waitcnt lgkmcnt(0)
	v_cmp_ge_u32_e32 vcc, s33, v176
	ds_read_b32 v230, v230
	v_lshl_add_u32 v149, v149, 6, v154
	v_cndmask_b32_e32 v148, v145, v148, vcc
	s_waitcnt lgkmcnt(0)
	v_cmp_ge_u32_e32 vcc, s33, v177
	ds_read_b32 v149, v149
	s_waitcnt lgkmcnt(0)
	ds_read_b128 v[234:237], v212
	v_cndmask_b32_e32 v245, v145, v230, vcc
	ds_read_b128 v[230:233], v211
	s_waitcnt lgkmcnt(0)
	v_mfma_f32_16x16x32_bf16 v[230:233], v[230:233], v[94:97], 0
	ds_read_b128 v[238:241], v212 offset:4096
	v_cmp_ge_u32_e32 vcc, s33, v178
	v_mfma_f32_16x16x32_bf16 v[230:233], v[234:237], v[90:93], v[230:233]
	ds_read_b128 v[234:237], v213
	v_cndmask_b32_e32 v149, v145, v149, vcc
	s_waitcnt lgkmcnt(0)
	v_mfma_f32_16x16x32_bf16 v[230:233], v[234:237], v[78:81], v[230:233]
	ds_read_b128 v[234:237], v214
	s_waitcnt lgkmcnt(0)
	v_mfma_f32_16x16x32_bf16 v[230:233], v[234:237], v[70:73], v[230:233]
	ds_read_b128 v[234:237], v211 offset:4096
	s_nop 6
	v_add_f32_e32 v134, v134, v230
	s_waitcnt lgkmcnt(0)
	v_mfma_f32_16x16x32_bf16 v[234:237], v[234:237], v[94:97], 0
	v_add_f32_e32 v152, v152, v231
	v_max3_f32 v230, v134, s25, v152
	v_add_f32_e32 v232, v242, v232
	v_mfma_f32_16x16x32_bf16 v[234:237], v[238:241], v[90:93], v[234:237]
	ds_read_b128 v[238:241], v213 offset:4096
	v_add_f32_e32 v233, v243, v233
	v_max3_f32 v230, v230, v232, v233
	s_waitcnt lgkmcnt(0)
	v_mfma_f32_16x16x32_bf16 v[234:237], v[238:241], v[78:81], v[234:237]
	ds_read_b128 v[238:241], v214 offset:4096
	s_waitcnt lgkmcnt(0)
	v_mfma_f32_16x16x32_bf16 v[234:237], v[238:241], v[70:73], v[234:237]
	s_nop 7
	v_add_f32_e32 v234, v244, v234
	v_add_f32_e32 v148, v148, v235
	v_max3_f32 v230, v230, v234, v148
	v_add_f32_e32 v235, v245, v236
	v_add_f32_e32 v149, v149, v237
	v_max3_f32 v230, v230, v235, v149
	v_mov_b32_e32 v231, v230
	s_nop 1
	v_permlane16_swap_b32_e32 v230, v231
	v_max_f32_e32 v231, v231, v231
	v_max_f32_e32 v230, v230, v230
	v_max_f32_e32 v230, v230, v231
	v_mov_b32_e32 v231, v230
	s_nop 1
	v_permlane32_swap_b32_e32 v230, v231
	v_max3_f32 v231, v150, v230, v231
	v_sub_f32_e32 v134, v134, v231
	v_sub_f32_e32 v232, v232, v231
	v_mul_f32_e32 v134, 0x3fb8aa3b, v134
	v_sub_f32_e32 v152, v152, v231
	v_mul_f32_e32 v232, 0x3fb8aa3b, v232
	v_exp_f32_e32 v134, v134
	v_mul_f32_e32 v152, 0x3fb8aa3b, v152
	v_exp_f32_e32 v236, v232
	v_sub_f32_e32 v232, v233, v231
	v_exp_f32_e32 v152, v152
	v_mul_f32_e32 v232, 0x3fb8aa3b, v232
	v_exp_f32_e32 v233, v232
	v_sub_f32_e32 v232, v234, v231
	v_mul_f32_e32 v232, 0x3fb8aa3b, v232
	v_sub_f32_e32 v148, v148, v231
	v_add_f32_e32 v230, 0, v134
	v_exp_f32_e32 v234, v232
	v_mul_f32_e32 v148, 0x3fb8aa3b, v148
	v_add_f32_e32 v230, v152, v230
	v_exp_f32_e32 v237, v148
	v_add_f32_e32 v230, v236, v230
	v_add_f32_e32 v230, v233, v230
	v_add_f32_e32 v230, v234, v230
	v_add_f32_e32 v148, v237, v230
	v_sub_f32_e32 v230, v235, v231
	v_mul_f32_e32 v230, 0x3fb8aa3b, v230
	v_sub_f32_e32 v149, v149, v231
	v_exp_f32_e32 v235, v230
	v_mul_f32_e32 v149, 0x3fb8aa3b, v149
	v_exp_f32_e32 v238, v149
	v_sub_f32_e32 v150, v150, v231
	v_add_f32_e32 v148, v235, v148
	v_mul_f32_e32 v150, 0x3fb8aa3b, v150
	v_add_f32_e32 v149, v238, v148
	v_exp_f32_e32 v148, v150
	v_mov_b32_e32 v150, v149
	s_nop 1
	v_permlane16_swap_b32_e32 v149, v150
	v_cvt_pk_bf16_f32 v232, v134, v152
	v_cvt_pk_bf16_f32 v233, v236, v233
	v_cvt_pk_bf16_f32 v234, v234, v237
	v_cvt_pk_bf16_f32 v235, v235, v238
	ds_read_b64_tr_b16 v[236:237], v215
	ds_read_b64_tr_b16 v[238:239], v215 offset:4096
	v_add_f32_e32 v149, v149, v150
	v_mov_b32_e32 v230, v149
	s_nop 1
	v_permlane32_swap_b32_e32 v149, v230
	v_mul_f32_e32 v102, v102, v148
	v_mul_f32_e32 v103, v103, v148
	v_mul_f32_e32 v100, v100, v148
	v_mul_f32_e32 v101, v101, v148
	v_mul_f32_e32 v106, v106, v148
	v_mul_f32_e32 v107, v107, v148
	v_mul_f32_e32 v104, v104, v148
	v_mul_f32_e32 v105, v105, v148
	s_waitcnt lgkmcnt(0)
	v_mfma_f32_16x16x32_bf16 v[100:103], v[236:239], v[232:235], v[100:103]
	ds_read_b64_tr_b16 v[236:237], v216
	ds_read_b64_tr_b16 v[238:239], v216 offset:4096
	v_mul_f32_e32 v110, v110, v148
	v_mul_f32_e32 v111, v111, v148
	v_mul_f32_e32 v108, v108, v148
	v_mul_f32_e32 v109, v109, v148
	s_waitcnt lgkmcnt(0)
	v_mfma_f32_16x16x32_bf16 v[104:107], v[236:239], v[232:235], v[104:107]
	ds_read_b64_tr_b16 v[236:237], v217
	ds_read_b64_tr_b16 v[238:239], v217 offset:4096
	v_mul_f32_e32 v114, v114, v148
	v_mul_f32_e32 v115, v115, v148
	v_mul_f32_e32 v112, v112, v148
	v_mul_f32_e32 v113, v113, v148
	s_waitcnt lgkmcnt(0)
	v_mfma_f32_16x16x32_bf16 v[108:111], v[236:239], v[232:235], v[108:111]
	ds_read_b64_tr_b16 v[236:237], v218
	ds_read_b64_tr_b16 v[238:239], v218 offset:4096
	v_mul_f32_e32 v118, v118, v148
	v_mul_f32_e32 v119, v119, v148
	v_mul_f32_e32 v116, v116, v148
	v_mul_f32_e32 v117, v117, v148
	s_waitcnt lgkmcnt(0)
	v_mfma_f32_16x16x32_bf16 v[112:115], v[236:239], v[232:235], v[112:115]
	ds_read_b64_tr_b16 v[236:237], v219
	ds_read_b64_tr_b16 v[238:239], v219 offset:4096
	v_mul_f32_e32 v122, v122, v148
	v_mul_f32_e32 v123, v123, v148
	v_mul_f32_e32 v120, v120, v148
	v_mul_f32_e32 v121, v121, v148
	s_waitcnt lgkmcnt(0)
	v_mfma_f32_16x16x32_bf16 v[116:119], v[236:239], v[232:235], v[116:119]
	ds_read_b64_tr_b16 v[236:237], v220
	ds_read_b64_tr_b16 v[238:239], v220 offset:4096
	v_mul_f32_e32 v126, v126, v148
	v_mul_f32_e32 v127, v127, v148
	v_mul_f32_e32 v124, v124, v148
	v_mul_f32_e32 v125, v125, v148
	s_waitcnt lgkmcnt(0)
	v_mfma_f32_16x16x32_bf16 v[120:123], v[236:239], v[232:235], v[120:123]
	ds_read_b64_tr_b16 v[236:237], v221
	ds_read_b64_tr_b16 v[238:239], v221 offset:4096
	v_mul_f32_e32 v130, v130, v148
	v_mul_f32_e32 v131, v131, v148
	v_mul_f32_e32 v128, v128, v148
	v_mul_f32_e32 v129, v129, v148
	s_waitcnt lgkmcnt(0)
	v_mfma_f32_16x16x32_bf16 v[124:127], v[236:239], v[232:235], v[124:127]
	ds_read_b64_tr_b16 v[236:237], v222
	ds_read_b64_tr_b16 v[238:239], v222 offset:4096
	ds_write_b128 v203, v[10:13]
	ds_write_b128 v204, v[14:17]
	ds_write_b128 v205, v[26:29]
	ds_write_b128 v206, v[30:33]
	ds_write_b128 v207, v[42:45]
	ds_write_b128 v208, v[46:49]
	ds_write_b128 v209, v[82:85]
	ds_write_b128 v210, v[86:89]
	s_waitcnt lgkmcnt(8)
	v_mfma_f32_16x16x32_bf16 v[128:131], v[236:239], v[232:235], v[128:131]
	s_cbranch_scc1 .LBB0_1986
	s_and_b32 s4, s34, 0x1fffffff
	s_mul_i32 s4, s4, s16
	s_add_i32 s4, s4, s14
	s_ashr_i32 s34, s4, 13
	s_ashr_i32 s35, s34, 31
	s_and_b32 s4, s15, 0x100
	s_lshl_b64 s[34:35], s[34:35], 21
	v_lshl_add_u32 v10, s4, 1, v151
	v_lshl_add_u64 v[82:83], v[140:141], 0, s[34:35]
	ds_read_u16 v11, v10 offset:448
	ds_read_u16 v12, v10 offset:456
	ds_read_u16 v26, v10 offset:464
	ds_read_u16 v28, v10 offset:472
	ds_read_u16 v42, v10 offset:480
	ds_read_u16 v44, v10 offset:488
	ds_read_u16 v84, v10 offset:496
	ds_read_u16 v86, v10 offset:504
	s_waitcnt lgkmcnt(7)
	v_lshlrev_b32_e32 v134, 8, v11
	v_lshl_add_u64 v[10:11], v[82:83], 0, v[134:135]
	s_waitcnt lgkmcnt(6)
	v_lshlrev_b32_e32 v134, 8, v12
	v_lshl_add_u64 v[14:15], v[82:83], 0, v[134:135]
	s_waitcnt lgkmcnt(5)
	v_lshlrev_b32_e32 v134, 8, v26
	v_lshl_add_u64 v[26:27], v[82:83], 0, v[134:135]
	s_waitcnt lgkmcnt(4)
	v_lshlrev_b32_e32 v134, 8, v28
	v_lshl_add_u64 v[30:31], v[82:83], 0, v[134:135]
	s_waitcnt lgkmcnt(3)
	v_lshlrev_b32_e32 v134, 8, v42
	v_lshl_add_u64 v[42:43], v[82:83], 0, v[134:135]
	s_waitcnt lgkmcnt(2)
	v_lshlrev_b32_e32 v134, 8, v44
	v_lshl_add_u64 v[46:47], v[82:83], 0, v[134:135]
	s_waitcnt lgkmcnt(1)
	v_lshlrev_b32_e32 v134, 8, v84
	v_lshl_add_u64 v[84:85], v[82:83], 0, v[134:135]
	s_waitcnt lgkmcnt(0)
	v_lshlrev_b32_e32 v134, 8, v86
	v_lshl_add_u64 v[86:87], v[82:83], 0, v[134:135]
	global_load_dwordx4 v[10:13], v[10:11], off
	s_nop 0
	global_load_dwordx4 v[14:17], v[14:15], off
	s_nop 0
	global_load_dwordx4 v[26:29], v[26:27], off
	s_nop 0
	global_load_dwordx4 v[30:33], v[30:31], off
	s_nop 0
	global_load_dwordx4 v[42:45], v[42:43], off
	s_nop 0
	global_load_dwordx4 v[46:49], v[46:47], off
	s_nop 0
	global_load_dwordx4 v[82:85], v[84:85], off
	s_nop 0
	global_load_dwordx4 v[86:89], v[86:87], off
.LBB0_1986:
	ds_read_b64 v[232:233], v223 offset:320
	v_cmp_ge_u32_e32 vcc, s33, v179
	s_add_i32 s4, s28, -1
	s_cmp_ge_i32 s4, s27
	s_waitcnt lgkmcnt(0)
	v_sub_u32_sdwa v134, s31, v232 dst_sel:DWORD dst_unused:UNUSED_PAD src0_sel:DWORD src1_sel:WORD_0
	v_med3_i32 v134, v134, 0, v1
	v_sub_u32_sdwa v150, s31, v232 dst_sel:DWORD dst_unused:UNUSED_PAD src0_sel:DWORD src1_sel:WORD_1
	v_lshl_add_u32 v134, v134, 6, v154
	v_med3_i32 v150, v150, 0, v1
	v_sub_u32_sdwa v152, s31, v233 dst_sel:DWORD dst_unused:UNUSED_PAD src0_sel:DWORD src1_sel:WORD_0
	ds_read_b32 v134, v134
	v_lshl_add_u32 v150, v150, 6, v154
	v_med3_i32 v152, v152, 0, v1
	v_sub_u32_sdwa v232, s31, v233 dst_sel:DWORD dst_unused:UNUSED_PAD src0_sel:DWORD src1_sel:WORD_1
	s_waitcnt lgkmcnt(0)
	ds_read_b32 v150, v150
	v_lshl_add_u32 v152, v152, 6, v154
	v_med3_i32 v232, v232, 0, v1
	v_cndmask_b32_e32 v134, v145, v134, vcc
	s_waitcnt lgkmcnt(0)
	v_cmp_ge_u32_e32 vcc, s33, v180
	ds_read_b32 v152, v152
	v_lshl_add_u32 v232, v232, 6, v154
	v_cndmask_b32_e32 v150, v145, v150, vcc
	s_waitcnt lgkmcnt(0)
	v_cmp_ge_u32_e32 vcc, s33, v181
	ds_read_b32 v232, v232
	s_waitcnt lgkmcnt(0)
	v_cndmask_b32_e32 v152, v145, v152, vcc
	v_cmp_ge_u32_e32 vcc, s33, v182
	s_nop 1
	v_cndmask_b32_e32 v244, v145, v232, vcc
	ds_read_b64 v[232:233], v223 offset:352
	v_cmp_ge_u32_e32 vcc, s33, v183
	s_waitcnt lgkmcnt(0)
	v_sub_u32_sdwa v234, s31, v232 dst_sel:DWORD dst_unused:UNUSED_PAD src0_sel:DWORD src1_sel:WORD_0
	v_med3_i32 v234, v234, 0, v1
	v_sub_u32_sdwa v232, s31, v232 dst_sel:DWORD dst_unused:UNUSED_PAD src0_sel:DWORD src1_sel:WORD_1
	v_lshl_add_u32 v234, v234, 6, v154
	v_med3_i32 v232, v232, 0, v1
	ds_read_b32 v234, v234
	v_lshl_add_u32 v232, v232, 6, v154
	s_waitcnt lgkmcnt(0)
	ds_read_b32 v232, v232
	v_cndmask_b32_e32 v245, v145, v234, vcc
	s_waitcnt lgkmcnt(0)
	v_cmp_ge_u32_e32 vcc, s33, v184
	s_nop 1
	v_cndmask_b32_e32 v246, v145, v232, vcc
	v_sub_u32_sdwa v232, s31, v233 dst_sel:DWORD dst_unused:UNUSED_PAD src0_sel:DWORD src1_sel:WORD_0
	v_med3_i32 v232, v232, 0, v1
	v_lshl_add_u32 v232, v232, 6, v154
	ds_read_b32 v232, v232
	s_waitcnt lgkmcnt(0)
	v_cmp_ge_u32_e32 vcc, s33, v185
	s_nop 1
	v_cndmask_b32_e32 v247, v145, v232, vcc
	v_sub_u32_sdwa v232, s31, v233 dst_sel:DWORD dst_unused:UNUSED_PAD src0_sel:DWORD src1_sel:WORD_1
	v_med3_i32 v232, v232, 0, v1
	v_lshl_add_u32 v232, v232, 6, v154
	ds_read_b32 v232, v232
	s_waitcnt lgkmcnt(0)
	v_cmp_ge_u32_e32 vcc, s33, v186
	ds_read_b128 v[236:239], v212
	ds_read_b128 v[240:243], v212 offset:4096
	v_cndmask_b32_e32 v248, v145, v232, vcc
	ds_read_b128 v[232:235], v211
	s_waitcnt lgkmcnt(0)
	v_mfma_f32_16x16x32_bf16 v[232:235], v[232:235], v[94:97], 0
	v_mfma_f32_16x16x32_bf16 v[232:235], v[236:239], v[90:93], v[232:235]
	ds_read_b128 v[236:239], v213
	s_waitcnt lgkmcnt(0)
	v_mfma_f32_16x16x32_bf16 v[232:235], v[236:239], v[78:81], v[232:235]
	ds_read_b128 v[236:239], v214
	s_waitcnt lgkmcnt(0)
	v_mfma_f32_16x16x32_bf16 v[232:235], v[236:239], v[70:73], v[232:235]
	ds_read_b128 v[236:239], v211 offset:4096
	s_nop 6
	v_add_f32_e32 v134, v134, v232
	s_waitcnt lgkmcnt(0)
	v_mfma_f32_16x16x32_bf16 v[236:239], v[236:239], v[94:97], 0
	v_add_f32_e32 v150, v150, v233
	v_max3_f32 v232, v134, s25, v150
	v_add_f32_e32 v233, v152, v234
	v_mfma_f32_16x16x32_bf16 v[236:239], v[240:243], v[90:93], v[236:239]
	ds_read_b128 v[240:243], v213 offset:4096
	v_add_f32_e32 v234, v244, v235
	v_max3_f32 v152, v232, v233, v234
	s_waitcnt lgkmcnt(0)
	v_mfma_f32_16x16x32_bf16 v[236:239], v[240:243], v[78:81], v[236:239]
	ds_read_b128 v[240:243], v214 offset:4096
	s_waitcnt lgkmcnt(0)
	v_mfma_f32_16x16x32_bf16 v[236:239], v[240:243], v[70:73], v[236:239]
	s_nop 7
	v_add_f32_e32 v232, v245, v236
	v_add_f32_e32 v235, v246, v237
	v_max3_f32 v152, v152, v232, v235
	v_add_f32_e32 v236, v247, v238
	v_add_f32_e32 v237, v248, v239
	v_max3_f32 v152, v152, v236, v237
	v_mov_b32_e32 v238, v152
	s_nop 1
	v_permlane16_swap_b32_e32 v152, v238
	v_max_f32_e32 v238, v238, v238
	v_max_f32_e32 v152, v152, v152
	v_max_f32_e32 v152, v152, v238
	v_mov_b32_e32 v238, v152
	s_nop 1
	v_permlane32_swap_b32_e32 v152, v238
	v_max3_f32 v152, v231, v152, v238
	v_sub_f32_e32 v134, v134, v152
	v_mul_f32_e32 v134, 0x3fb8aa3b, v134
	v_sub_f32_e32 v150, v150, v152
	v_exp_f32_e32 v134, v134
	v_mul_f32_e32 v150, 0x3fb8aa3b, v150
	v_exp_f32_e32 v239, v150
	v_sub_f32_e32 v232, v232, v152
	v_sub_f32_e32 v233, v233, v152
	v_mul_f32_e32 v232, 0x3fb8aa3b, v232
	v_mul_f32_e32 v233, 0x3fb8aa3b, v233
	v_sub_f32_e32 v234, v234, v152
	v_exp_f32_e32 v240, v232
	v_sub_f32_e32 v232, v235, v152
	v_add_f32_e32 v238, 0, v134
	v_exp_f32_e32 v233, v233
	v_mul_f32_e32 v234, 0x3fb8aa3b, v234
	v_mul_f32_e32 v232, 0x3fb8aa3b, v232
	v_add_f32_e32 v150, v239, v238
	v_exp_f32_e32 v238, v234
	v_exp_f32_e32 v241, v232
	v_sub_f32_e32 v232, v236, v152
	v_mul_f32_e32 v232, 0x3fb8aa3b, v232
	v_exp_f32_e32 v242, v232
	v_sub_f32_e32 v232, v237, v152
	v_add_f32_e32 v150, v233, v150
	v_mul_f32_e32 v232, 0x3fb8aa3b, v232
	v_add_f32_e32 v150, v238, v150
	v_exp_f32_e32 v237, v232
	v_add_f32_e32 v150, v240, v150
	v_sub_f32_e32 v231, v231, v152
	v_add_f32_e32 v150, v241, v150
	v_mul_f32_e32 v231, 0x3fb8aa3b, v231
	v_add_f32_e32 v150, v242, v150
	v_add_f32_e32 v232, v237, v150
	v_exp_f32_e32 v150, v231
	v_cvt_pk_bf16_f32 v234, v134, v239
	v_cvt_pk_bf16_f32 v235, v233, v238
	v_cvt_pk_bf16_f32 v236, v240, v241
	v_cvt_pk_bf16_f32 v237, v242, v237
	ds_read_b64_tr_b16 v[238:239], v215
	ds_read_b64_tr_b16 v[240:241], v215 offset:4096
	v_mul_f32_e32 v102, v102, v150
	v_mul_f32_e32 v103, v103, v150
	v_mul_f32_e32 v100, v100, v150
	v_mul_f32_e32 v101, v101, v150
	v_mul_f32_e32 v106, v106, v150
	v_mul_f32_e32 v107, v107, v150
	v_mul_f32_e32 v104, v104, v150
	v_mul_f32_e32 v105, v105, v150
	s_waitcnt lgkmcnt(0)
	v_mfma_f32_16x16x32_bf16 v[100:103], v[238:241], v[234:237], v[100:103]
	ds_read_b64_tr_b16 v[238:239], v216
	ds_read_b64_tr_b16 v[240:241], v216 offset:4096
	v_mul_f32_e32 v110, v110, v150
	v_mul_f32_e32 v111, v111, v150
	v_mul_f32_e32 v108, v108, v150
	v_mul_f32_e32 v109, v109, v150
	s_waitcnt lgkmcnt(0)
	v_mfma_f32_16x16x32_bf16 v[104:107], v[238:241], v[234:237], v[104:107]
	ds_read_b64_tr_b16 v[238:239], v217
	ds_read_b64_tr_b16 v[240:241], v217 offset:4096
	v_mul_f32_e32 v114, v114, v150
	v_mul_f32_e32 v115, v115, v150
	v_mul_f32_e32 v112, v112, v150
	v_mul_f32_e32 v113, v113, v150
	s_waitcnt lgkmcnt(0)
	v_mfma_f32_16x16x32_bf16 v[108:111], v[238:241], v[234:237], v[108:111]
	ds_read_b64_tr_b16 v[238:239], v218
	ds_read_b64_tr_b16 v[240:241], v218 offset:4096
	v_mul_f32_e32 v118, v118, v150
	v_mul_f32_e32 v119, v119, v150
	v_mul_f32_e32 v116, v116, v150
	v_mul_f32_e32 v117, v117, v150
	s_waitcnt lgkmcnt(0)
	v_mfma_f32_16x16x32_bf16 v[112:115], v[238:241], v[234:237], v[112:115]
	ds_read_b64_tr_b16 v[238:239], v219
	ds_read_b64_tr_b16 v[240:241], v219 offset:4096
	v_mul_f32_e32 v122, v122, v150
	v_mul_f32_e32 v123, v123, v150
	v_mul_f32_e32 v120, v120, v150
	v_mul_f32_e32 v121, v121, v150
	s_waitcnt lgkmcnt(0)
	v_mfma_f32_16x16x32_bf16 v[116:119], v[238:241], v[234:237], v[116:119]
	ds_read_b64_tr_b16 v[238:239], v220
	ds_read_b64_tr_b16 v[240:241], v220 offset:4096
	v_mul_f32_e32 v126, v126, v150
	v_mul_f32_e32 v127, v127, v150
	v_mul_f32_e32 v124, v124, v150
	v_mul_f32_e32 v125, v125, v150
	s_waitcnt lgkmcnt(0)
	v_mfma_f32_16x16x32_bf16 v[120:123], v[238:241], v[234:237], v[120:123]
	ds_read_b64_tr_b16 v[238:239], v221
	ds_read_b64_tr_b16 v[240:241], v221 offset:4096
	v_mov_b32_e32 v231, v232
	v_mul_f32_e32 v130, v130, v150
	v_mul_f32_e32 v131, v131, v150
	s_waitcnt lgkmcnt(0)
	v_mfma_f32_16x16x32_bf16 v[124:127], v[238:241], v[234:237], v[124:127]
	ds_read_b64_tr_b16 v[238:239], v222
	ds_read_b64_tr_b16 v[240:241], v222 offset:4096
	v_mul_f32_e32 v128, v128, v150
	v_mul_f32_e32 v129, v129, v150
	v_permlane16_swap_b32_e32 v232, v231
	s_waitcnt lgkmcnt(0)
	v_mfma_f32_16x16x32_bf16 v[128:131], v[238:241], v[234:237], v[128:131]
	v_add_f32_e32 v231, v232, v231
	v_mov_b32_e32 v232, v231
	s_nop 1
	v_permlane32_swap_b32_e32 v231, v232
	s_waitcnt vmcnt(7)
	ds_write_b128 v203, v[2:5]
	s_waitcnt vmcnt(6)
	ds_write_b128 v204, v[6:9]
	s_waitcnt vmcnt(5)
	ds_write_b128 v205, v[18:21]
	s_waitcnt vmcnt(4)
	ds_write_b128 v206, v[22:25]
	s_waitcnt vmcnt(3)
	ds_write_b128 v207, v[34:37]
	s_waitcnt vmcnt(2)
	ds_write_b128 v208, v[38:41]
	s_waitcnt vmcnt(1)
	ds_write_b128 v209, v[50:53]
	s_waitcnt vmcnt(0)
	ds_write_b128 v210, v[54:57]
	s_cbranch_scc1 .LBB0_1988
	s_lshr_b32 s4, s4, 3
	s_mul_i32 s4, s4, s16
	s_add_i32 s4, s4, s14
	s_ashr_i32 s34, s4, 13
	s_add_i32 s4, s15, 0x100
	s_ashr_i32 s35, s34, 31
	s_and_b32 s4, s4, 0x100
	s_lshl_b64 s[34:35], s[34:35], 21
	v_lshl_add_u32 v2, s4, 1, v151
	v_lshl_add_u64 v[50:51], v[140:141], 0, s[34:35]
	ds_read_u16 v3, v2
	ds_read_u16 v4, v2 offset:8
	ds_read_u16 v18, v2 offset:16
	ds_read_u16 v20, v2 offset:24
	ds_read_u16 v34, v2 offset:32
	ds_read_u16 v36, v2 offset:40
	ds_read_u16 v52, v2 offset:48
	ds_read_u16 v54, v2 offset:56
	s_waitcnt lgkmcnt(7)
	v_lshlrev_b32_e32 v134, 8, v3
	v_lshl_add_u64 v[2:3], v[50:51], 0, v[134:135]
	s_waitcnt lgkmcnt(6)
	v_lshlrev_b32_e32 v134, 8, v4
	v_lshl_add_u64 v[6:7], v[50:51], 0, v[134:135]
	s_waitcnt lgkmcnt(5)
	v_lshlrev_b32_e32 v134, 8, v18
	v_lshl_add_u64 v[18:19], v[50:51], 0, v[134:135]
	s_waitcnt lgkmcnt(4)
	v_lshlrev_b32_e32 v134, 8, v20
	v_lshl_add_u64 v[22:23], v[50:51], 0, v[134:135]
	s_waitcnt lgkmcnt(3)
	v_lshlrev_b32_e32 v134, 8, v34
	v_lshl_add_u64 v[34:35], v[50:51], 0, v[134:135]
	s_waitcnt lgkmcnt(2)
	v_lshlrev_b32_e32 v134, 8, v36
	v_lshl_add_u64 v[38:39], v[50:51], 0, v[134:135]
	s_waitcnt lgkmcnt(1)
	v_lshlrev_b32_e32 v134, 8, v52
	v_lshl_add_u64 v[52:53], v[50:51], 0, v[134:135]
	s_waitcnt lgkmcnt(0)
	v_lshlrev_b32_e32 v134, 8, v54
	v_lshl_add_u64 v[54:55], v[50:51], 0, v[134:135]
	global_load_dwordx4 v[2:5], v[2:3], off
	s_nop 0
	global_load_dwordx4 v[6:9], v[6:7], off
	s_nop 0
	global_load_dwordx4 v[18:21], v[18:19], off
	s_nop 0
	global_load_dwordx4 v[22:25], v[22:23], off
	s_nop 0
	global_load_dwordx4 v[34:37], v[34:35], off
	s_nop 0
	global_load_dwordx4 v[38:41], v[38:39], off
	s_nop 0
	global_load_dwordx4 v[50:53], v[52:53], off
	s_nop 0
	global_load_dwordx4 v[54:57], v[54:55], off
.LBB0_1988:
	ds_read_b64 v[234:235], v223 offset:384
	v_cmp_ge_u32_e32 vcc, s33, v187
	s_cmp_ge_i32 s28, s27
	s_waitcnt lgkmcnt(0)
	v_sub_u32_sdwa v134, s31, v234 dst_sel:DWORD dst_unused:UNUSED_PAD src0_sel:DWORD src1_sel:WORD_0
	v_med3_i32 v134, v134, 0, v1
	v_sub_u32_sdwa v233, s31, v234 dst_sel:DWORD dst_unused:UNUSED_PAD src0_sel:DWORD src1_sel:WORD_1
	v_lshl_add_u32 v134, v134, 6, v154
	v_med3_i32 v233, v233, 0, v1
	v_sub_u32_sdwa v234, s31, v235 dst_sel:DWORD dst_unused:UNUSED_PAD src0_sel:DWORD src1_sel:WORD_0
	ds_read_b32 v134, v134
	v_lshl_add_u32 v233, v233, 6, v154
	v_med3_i32 v234, v234, 0, v1
	s_waitcnt lgkmcnt(0)
	ds_read_b32 v233, v233
	v_lshl_add_u32 v234, v234, 6, v154
	v_cndmask_b32_e32 v134, v145, v134, vcc
	s_waitcnt lgkmcnt(0)
	v_cmp_gt_u32_e32 vcc, s33, v187
	ds_read_b32 v234, v234
	s_waitcnt lgkmcnt(0)
	v_cndmask_b32_e32 v233, v145, v233, vcc
	v_cmp_ge_u32_e32 vcc, s33, v188
	s_nop 1
	v_cndmask_b32_e32 v246, v145, v234, vcc
	v_sub_u32_sdwa v234, s31, v235 dst_sel:DWORD dst_unused:UNUSED_PAD src0_sel:DWORD src1_sel:WORD_1
	v_med3_i32 v234, v234, 0, v1
	v_lshl_add_u32 v234, v234, 6, v154
	ds_read_b32 v234, v234
	s_waitcnt lgkmcnt(0)
	v_cmp_ge_u32_e32 vcc, s33, v189
	s_nop 1
	v_cndmask_b32_e32 v247, v145, v234, vcc
	ds_read_b64 v[234:235], v223 offset:416
	v_cmp_ge_u32_e32 vcc, s33, v190
	s_waitcnt lgkmcnt(0)
	v_sub_u32_sdwa v236, s31, v234 dst_sel:DWORD dst_unused:UNUSED_PAD src0_sel:DWORD src1_sel:WORD_0
	v_med3_i32 v236, v236, 0, v1
	v_sub_u32_sdwa v234, s31, v234 dst_sel:DWORD dst_unused:UNUSED_PAD src0_sel:DWORD src1_sel:WORD_1
	v_lshl_add_u32 v236, v236, 6, v154
	v_med3_i32 v234, v234, 0, v1
	ds_read_b32 v236, v236
	v_lshl_add_u32 v234, v234, 6, v154
	s_waitcnt lgkmcnt(0)
	ds_read_b32 v234, v234
	v_cndmask_b32_e32 v248, v145, v236, vcc
	s_waitcnt lgkmcnt(0)
	v_cmp_ge_u32_e32 vcc, s33, v191
	s_nop 1
	v_cndmask_b32_e32 v249, v145, v234, vcc
	v_sub_u32_sdwa v234, s31, v235 dst_sel:DWORD dst_unused:UNUSED_PAD src0_sel:DWORD src1_sel:WORD_0
	v_med3_i32 v234, v234, 0, v1
	v_lshl_add_u32 v234, v234, 6, v154
	ds_read_b32 v234, v234
	s_waitcnt lgkmcnt(0)
	v_cmp_ge_u32_e32 vcc, s33, v192
	s_nop 1
	v_cndmask_b32_e32 v250, v145, v234, vcc
	v_sub_u32_sdwa v234, s31, v235 dst_sel:DWORD dst_unused:UNUSED_PAD src0_sel:DWORD src1_sel:WORD_1
	v_med3_i32 v234, v234, 0, v1
	v_lshl_add_u32 v234, v234, 6, v154
	ds_read_b32 v234, v234
	s_waitcnt lgkmcnt(0)
	v_cmp_ge_u32_e32 vcc, s33, v193
	ds_read_b128 v[238:241], v212
	ds_read_b128 v[242:245], v212 offset:4096
	v_cndmask_b32_e32 v251, v145, v234, vcc
	ds_read_b128 v[234:237], v211
	s_waitcnt lgkmcnt(0)
	v_mfma_f32_16x16x32_bf16 v[234:237], v[234:237], v[94:97], 0
	v_mfma_f32_16x16x32_bf16 v[234:237], v[238:241], v[90:93], v[234:237]
	ds_read_b128 v[238:241], v213
	s_waitcnt lgkmcnt(0)
	v_mfma_f32_16x16x32_bf16 v[234:237], v[238:241], v[78:81], v[234:237]
	ds_read_b128 v[238:241], v214
	s_waitcnt lgkmcnt(0)
	v_mfma_f32_16x16x32_bf16 v[234:237], v[238:241], v[70:73], v[234:237]
	ds_read_b128 v[238:241], v211 offset:4096
	s_nop 6
	v_add_f32_e32 v134, v134, v234
	s_waitcnt lgkmcnt(0)
	v_mfma_f32_16x16x32_bf16 v[238:241], v[238:241], v[94:97], 0
	v_add_f32_e32 v234, v233, v235
	v_max3_f32 v233, v134, s25, v234
	v_add_f32_e32 v235, v246, v236
	v_mfma_f32_16x16x32_bf16 v[238:241], v[242:245], v[90:93], v[238:241]
	ds_read_b128 v[242:245], v213 offset:4096
	v_add_f32_e32 v236, v247, v237
	v_max3_f32 v233, v233, v235, v236
	s_waitcnt lgkmcnt(0)
	v_mfma_f32_16x16x32_bf16 v[238:241], v[242:245], v[78:81], v[238:241]
	ds_read_b128 v[242:245], v214 offset:4096
	s_waitcnt lgkmcnt(0)
	v_mfma_f32_16x16x32_bf16 v[238:241], v[242:245], v[70:73], v[238:241]
	s_nop 7
	v_add_f32_e32 v237, v248, v238
	v_add_f32_e32 v238, v249, v239
	v_max3_f32 v233, v233, v237, v238
	v_add_f32_e32 v239, v250, v240
	v_add_f32_e32 v240, v251, v241
	v_max3_f32 v233, v233, v239, v240
	v_mov_b32_e32 v241, v233
	s_nop 1
	v_permlane16_swap_b32_e32 v233, v241
	v_max_f32_e32 v241, v241, v241
	v_max_f32_e32 v233, v233, v233
	v_max_f32_e32 v233, v233, v241
	v_mov_b32_e32 v241, v233
	s_nop 1
	v_permlane32_swap_b32_e32 v233, v241
	v_max3_f32 v233, v152, v233, v241
	v_sub_f32_e32 v134, v134, v233
	v_mul_f32_e32 v134, 0x3fb8aa3b, v134
	v_sub_f32_e32 v234, v234, v233
	v_exp_f32_e32 v134, v134
	v_mul_f32_e32 v234, 0x3fb8aa3b, v234
	v_exp_f32_e32 v242, v234
	v_sub_f32_e32 v235, v235, v233
	v_add_f32_e32 v241, 0, v134
	v_mul_f32_e32 v235, 0x3fb8aa3b, v235
	v_add_f32_e32 v234, v242, v241
	v_exp_f32_e32 v241, v235
	v_sub_f32_e32 v235, v236, v233
	v_mul_f32_e32 v235, 0x3fb8aa3b, v235
	v_exp_f32_e32 v243, v235
	v_sub_f32_e32 v235, v237, v233
	v_mul_f32_e32 v235, 0x3fb8aa3b, v235
	v_exp_f32_e32 v244, v235
	v_sub_f32_e32 v235, v238, v233
	v_mul_f32_e32 v235, 0x3fb8aa3b, v235
	v_exp_f32_e32 v238, v235
	v_sub_f32_e32 v235, v239, v233
	v_mul_f32_e32 v235, 0x3fb8aa3b, v235
	v_exp_f32_e32 v239, v235
	v_sub_f32_e32 v235, v240, v233
	v_add_f32_e32 v234, v241, v234
	v_mul_f32_e32 v235, 0x3fb8aa3b, v235
	v_add_f32_e32 v234, v243, v234
	v_exp_f32_e32 v240, v235
	v_add_f32_e32 v234, v244, v234
	v_sub_f32_e32 v152, v152, v233
	v_add_f32_e32 v234, v238, v234
	v_mul_f32_e32 v152, 0x3fb8aa3b, v152
	v_add_f32_e32 v234, v239, v234
	v_add_f32_e32 v234, v240, v234
	v_exp_f32_e32 v152, v152
	v_cvt_pk_bf16_f32 v236, v134, v242
	v_cvt_pk_bf16_f32 v237, v241, v243
	v_cvt_pk_bf16_f32 v238, v244, v238
	v_cvt_pk_bf16_f32 v239, v239, v240
	ds_read_b64_tr_b16 v[240:241], v215
	ds_read_b64_tr_b16 v[242:243], v215 offset:4096
	v_mul_f32_e32 v102, v102, v152
	v_mul_f32_e32 v103, v103, v152
	v_mul_f32_e32 v100, v100, v152
	v_mul_f32_e32 v101, v101, v152
	v_mul_f32_e32 v106, v106, v152
	v_mul_f32_e32 v107, v107, v152
	v_mul_f32_e32 v104, v104, v152
	v_mul_f32_e32 v105, v105, v152
	s_waitcnt lgkmcnt(0)
	v_mfma_f32_16x16x32_bf16 v[100:103], v[240:243], v[236:239], v[100:103]
	ds_read_b64_tr_b16 v[240:241], v216
	ds_read_b64_tr_b16 v[242:243], v216 offset:4096
	v_mul_f32_e32 v110, v110, v152
	v_mul_f32_e32 v111, v111, v152
	v_mul_f32_e32 v108, v108, v152
	v_mul_f32_e32 v109, v109, v152
	s_waitcnt lgkmcnt(0)
	v_mfma_f32_16x16x32_bf16 v[104:107], v[240:243], v[236:239], v[104:107]
	ds_read_b64_tr_b16 v[240:241], v217
	ds_read_b64_tr_b16 v[242:243], v217 offset:4096
	v_mul_f32_e32 v114, v114, v152
	v_mul_f32_e32 v115, v115, v152
	v_mul_f32_e32 v112, v112, v152
	v_mul_f32_e32 v113, v113, v152
	s_waitcnt lgkmcnt(0)
	v_mfma_f32_16x16x32_bf16 v[108:111], v[240:243], v[236:239], v[108:111]
	ds_read_b64_tr_b16 v[240:241], v218
	ds_read_b64_tr_b16 v[242:243], v218 offset:4096
	v_mul_f32_e32 v118, v118, v152
	v_mul_f32_e32 v119, v119, v152
	v_mul_f32_e32 v116, v116, v152
	v_mul_f32_e32 v117, v117, v152
	s_waitcnt lgkmcnt(0)
	v_mfma_f32_16x16x32_bf16 v[112:115], v[240:243], v[236:239], v[112:115]
	ds_read_b64_tr_b16 v[240:241], v219
	ds_read_b64_tr_b16 v[242:243], v219 offset:4096
	v_mul_f32_e32 v122, v122, v152
	v_mul_f32_e32 v123, v123, v152
	v_mul_f32_e32 v120, v120, v152
	v_mul_f32_e32 v121, v121, v152
	s_waitcnt lgkmcnt(0)
	v_mfma_f32_16x16x32_bf16 v[116:119], v[240:243], v[236:239], v[116:119]
	ds_read_b64_tr_b16 v[240:241], v220
	ds_read_b64_tr_b16 v[242:243], v220 offset:4096
	v_mul_f32_e32 v126, v126, v152
	v_mul_f32_e32 v127, v127, v152
	v_mul_f32_e32 v124, v124, v152
	v_mul_f32_e32 v125, v125, v152
	s_waitcnt lgkmcnt(0)
	v_mfma_f32_16x16x32_bf16 v[120:123], v[240:243], v[236:239], v[120:123]
	ds_read_b64_tr_b16 v[240:241], v221
	ds_read_b64_tr_b16 v[242:243], v221 offset:4096
	v_mov_b32_e32 v235, v234
	v_mul_f32_e32 v130, v130, v152
	v_mul_f32_e32 v131, v131, v152
	s_waitcnt lgkmcnt(0)
	v_mfma_f32_16x16x32_bf16 v[124:127], v[240:243], v[236:239], v[124:127]
	ds_read_b64_tr_b16 v[240:241], v222
	ds_read_b64_tr_b16 v[242:243], v222 offset:4096
	v_mul_f32_e32 v128, v128, v152
	v_mul_f32_e32 v129, v129, v152
	v_permlane16_swap_b32_e32 v234, v235
	s_waitcnt lgkmcnt(0)
	v_mfma_f32_16x16x32_bf16 v[128:131], v[240:243], v[236:239], v[128:131]
	v_add_f32_e32 v234, v234, v235
	v_mov_b32_e32 v235, v234
	s_nop 1
	v_permlane32_swap_b32_e32 v234, v235
	ds_write_b128 v203, v[10:13]
	ds_write_b128 v204, v[14:17]
	ds_write_b128 v205, v[26:29]
	ds_write_b128 v206, v[30:33]
	ds_write_b128 v207, v[42:45]
	ds_write_b128 v208, v[46:49]
	ds_write_b128 v209, v[82:85]
	ds_write_b128 v210, v[86:89]
	s_cbranch_scc1 .LBB0_1973
	s_lshr_b32 s4, s28, 3
	s_mul_i32 s4, s4, s16
	s_add_i32 s4, s4, s14
	s_ashr_i32 s34, s4, 13
	s_lshl_b32 s4, s28, 6
	s_ashr_i32 s35, s34, 31
	s_and_b32 s4, s4, 0x200
	s_lshl_b64 s[34:35], s[34:35], 21
	v_add_u32_e32 v10, s4, v151
	v_lshl_add_u64 v[82:83], v[140:141], 0, s[34:35]
	ds_read_u16 v11, v10 offset:64
	ds_read_u16 v12, v10 offset:72
	ds_read_u16 v26, v10 offset:80
	ds_read_u16 v28, v10 offset:88
	ds_read_u16 v42, v10 offset:96
	ds_read_u16 v44, v10 offset:104
	ds_read_u16 v84, v10 offset:112
	ds_read_u16 v86, v10 offset:120
	s_waitcnt lgkmcnt(7)
	v_lshlrev_b32_e32 v134, 8, v11
	v_lshl_add_u64 v[10:11], v[82:83], 0, v[134:135]
	s_waitcnt lgkmcnt(6)
	v_lshlrev_b32_e32 v134, 8, v12
	v_lshl_add_u64 v[14:15], v[82:83], 0, v[134:135]
	s_waitcnt lgkmcnt(5)
	v_lshlrev_b32_e32 v134, 8, v26
	v_lshl_add_u64 v[26:27], v[82:83], 0, v[134:135]
	s_waitcnt lgkmcnt(4)
	v_lshlrev_b32_e32 v134, 8, v28
	v_lshl_add_u64 v[30:31], v[82:83], 0, v[134:135]
	s_waitcnt lgkmcnt(3)
	v_lshlrev_b32_e32 v134, 8, v42
	v_lshl_add_u64 v[42:43], v[82:83], 0, v[134:135]
	s_waitcnt lgkmcnt(2)
	v_lshlrev_b32_e32 v134, 8, v44
	v_lshl_add_u64 v[46:47], v[82:83], 0, v[134:135]
	s_waitcnt lgkmcnt(1)
	v_lshlrev_b32_e32 v134, 8, v84
	v_lshl_add_u64 v[84:85], v[82:83], 0, v[134:135]
	s_waitcnt lgkmcnt(0)
	v_lshlrev_b32_e32 v134, 8, v86
	v_lshl_add_u64 v[86:87], v[82:83], 0, v[134:135]
	global_load_dwordx4 v[10:13], v[10:11], off
	s_nop 0
	global_load_dwordx4 v[14:17], v[14:15], off
	s_nop 0
	global_load_dwordx4 v[26:29], v[26:27], off
	s_nop 0
	global_load_dwordx4 v[30:33], v[30:31], off
	s_nop 0
	global_load_dwordx4 v[42:45], v[42:43], off
	s_nop 0
	global_load_dwordx4 v[46:49], v[46:47], off
	s_nop 0
	global_load_dwordx4 v[82:85], v[84:85], off
	s_nop 0
	global_load_dwordx4 v[86:89], v[86:87], off
	s_branch .LBB0_1973

.LBB0_2008:
	s_or_b64 exec, exec, s[26:27]
	s_waitcnt lgkmcnt(0)
	s_barrier
	ds_read_b128 v[38:41], v114 offset:33280
	ds_read_b128 v[42:45], v114 offset:33296
	s_mov_b32 s26, 0x358637bd
	s_waitcnt vmcnt(3)
	v_lshlrev_b32_e32 v52, 16, v148
	v_lshl_add_u64 v[48:49], s[46:47], 0, v[104:105]
	s_waitcnt lgkmcnt(1)
	v_mov_b32_e32 v46, v38
	s_waitcnt lgkmcnt(0)
	v_mov_b32_e32 v47, v42
	v_mov_b32_e32 v42, v39
	v_add_f32_e32 v38, v46, v42
	v_add_f32_e32 v39, v47, v43
	v_mov_b32_e32 v42, v40
	v_mov_b32_e32 v43, v44
	v_mov_b32_e32 v44, v41
	v_add_f32_e32 v40, v42, v44
	v_add_f32_e32 v41, v43, v45
	s_waitcnt vmcnt(1)
	v_lshlrev_b32_e32 v54, 16, v146
	v_add_f32_e32 v46, v38, v40
	v_add_f32_e32 v47, v39, v41
	ds_read_b128 v[38:41], v140 offset:33280
	ds_read_b128 v[42:45], v140 offset:33296
	v_add_u32_e32 v74, 0x4000, v74
	v_lshl_add_u64 v[102:103], v[102:103], 0, s[40:41]
	v_lshl_add_u64 v[104:105], v[104:105], 0, s[44:45]
	s_waitcnt lgkmcnt(1)
	v_mov_b32_e32 v50, v38
	s_waitcnt lgkmcnt(0)
	v_mov_b32_e32 v51, v42
	v_mov_b32_e32 v42, v39
	v_add_f32_e32 v38, v50, v42
	v_add_f32_e32 v39, v51, v43
	v_mov_b32_e32 v42, v40
	v_mov_b32_e32 v43, v44
	v_mov_b32_e32 v44, v41
	v_add_f32_e32 v40, v42, v44
	v_add_f32_e32 v41, v43, v45
	v_lshl_add_u64 v[108:109], v[108:109], 0, s[40:41]
	v_add_f32_e32 v38, v38, v40
	v_add_f32_e32 v39, v39, v41
	v_mov_b32_e32 v41, v46
	v_mov_b32_e32 v40, v38
	v_mov_b32_e32 v46, v39
	v_add_f32_e32 v38, v40, v46
	v_add_f32_e32 v39, v41, v47
	v_mov_b64_e32 v[46:47], s[26:27]
	v_pk_fma_f32 v[38:39], v[38:39], s[38:39], v[46:47] op_sel_hi:[1,0,0]
	s_cmp_eq_u32 s36, 64
	v_mul_f32_e32 v40, 0x4b800000, v39
	v_cmp_gt_f32_e64 s[28:29], s54, v39
	v_cmp_gt_f32_e64 s[26:27], s54, v38
	s_mov_b32 s61, s36
	v_cndmask_b32_e64 v39, v39, v40, s[28:29]
	v_rsq_f32_e32 v39, v39
	s_nop 0
	v_mul_f32_e32 v40, 0x45800000, v39
	v_cndmask_b32_e64 v39, v39, v40, s[28:29]
	v_mul_f32_e32 v34, v34, v39
	v_mul_f32_e32 v34, v144, v34
	v_mul_f32_e32 v34, v34, v52
	v_mul_f32_e32 v34, 0x41000000, v34
	v_mov_b32_e32 v39, 0
	v_cvt_pk_fp8_f32 v39, v34, v34
	v_mul_f32_e32 v34, 0x4b800000, v38
	v_cndmask_b32_e64 v34, v38, v34, s[26:27]
	v_rsq_f32_e32 v34, v34
	global_store_byte v[48:49], v39, off
	v_mul_f32_e32 v38, 0x45800000, v34
	v_cndmask_b32_e64 v34, v34, v38, s[26:27]
	v_mul_f32_e32 v34, v35, v34
	v_mul_f32_e32 v34, v144, v34
	v_lshlrev_b32_e32 v35, 16, v147
	v_mul_f32_e32 v34, v34, v35
	v_mul_f32_e32 v34, 0x41000000, v34
	v_mov_b32_e32 v38, 0
	v_cvt_pk_fp8_f32 v38, v34, v34
	v_lshl_add_u64 v[34:35], s[46:47], 0, v[106:107]
	s_mov_b32 s26, 0x3593a000
	v_add_co_u32_e64 v48, s[26:27], s26, v34
	v_lshl_add_u64 v[106:107], v[106:107], 0, s[44:45]
	s_nop 0
	v_addc_co_u32_e64 v49, s[26:27], 0, v35, s[26:27]
	global_store_byte v[48:49], v38, off
	ds_read_b128 v[38:41], v141 offset:33280
	ds_read_b128 v[42:45], v141 offset:33296
	s_waitcnt lgkmcnt(1)
	v_mov_b32_e32 v50, v38
	s_waitcnt lgkmcnt(0)
	v_mov_b32_e32 v51, v42
	v_mov_b32_e32 v42, v39
	v_add_f32_e32 v38, v50, v42
	v_add_f32_e32 v39, v51, v43
	v_mov_b32_e32 v42, v40
	v_mov_b32_e32 v43, v44
	v_mov_b32_e32 v44, v41
	v_add_f32_e32 v40, v42, v44
	v_add_f32_e32 v41, v43, v45
	s_nop 0
	v_add_f32_e32 v50, v38, v40
	v_add_f32_e32 v51, v39, v41
	ds_read_b128 v[38:41], v142 offset:33280
	ds_read_b128 v[42:45], v142 offset:33296
	s_waitcnt lgkmcnt(1)
	v_mov_b32_e32 v52, v38
	s_waitcnt lgkmcnt(0)
	v_mov_b32_e32 v53, v42
	v_mov_b32_e32 v42, v39
	v_add_f32_e32 v38, v52, v42
	v_add_f32_e32 v39, v53, v43
	v_mov_b32_e32 v42, v40
	v_mov_b32_e32 v43, v44
	v_mov_b32_e32 v44, v41
	v_add_f32_e32 v40, v42, v44
	v_add_f32_e32 v41, v43, v45
	s_nop 0
	v_add_f32_e32 v38, v38, v40
	v_add_f32_e32 v39, v39, v41
	v_mov_b32_e32 v41, v50
	v_mov_b32_e32 v40, v38
	v_mov_b32_e32 v50, v39
	v_add_f32_e32 v38, v40, v50
	v_add_f32_e32 v39, v41, v51
	s_nop 0
	v_pk_fma_f32 v[38:39], v[38:39], s[38:39], v[46:47] op_sel_hi:[1,0,0]
	s_nop 0
	v_mul_f32_e32 v40, 0x4b800000, v39
	v_cmp_gt_f32_e64 s[28:29], s54, v39
	v_cmp_gt_f32_e64 s[26:27], s54, v38
	s_nop 0
	v_cndmask_b32_e64 v39, v39, v40, s[28:29]
	v_rsq_f32_e32 v39, v39
	s_nop 0
	v_mul_f32_e32 v40, 0x45800000, v39
	v_cndmask_b32_e64 v39, v39, v40, s[28:29]
	v_mul_f32_e32 v36, v36, v39
	v_mul_f32_e32 v36, v144, v36
	v_mul_f32_e32 v36, v36, v54
	v_mul_f32_e32 v36, 0x41000000, v36
	v_mov_b32_e32 v39, 0
	v_cvt_pk_fp8_f32 v39, v36, v36
	v_mul_f32_e32 v36, 0x4b800000, v38
	v_cndmask_b32_e64 v36, v38, v36, s[26:27]
	v_rsq_f32_e32 v36, v36
	global_store_byte v[48:49], v39, off offset:3072
	v_mul_f32_e32 v38, 0x45800000, v36
	v_cndmask_b32_e64 v36, v36, v38, s[26:27]
	v_mul_f32_e32 v36, v37, v36
	v_mul_f32_e32 v36, v144, v36
	s_waitcnt vmcnt(3)
	v_lshlrev_b32_e32 v37, 16, v145
	v_mul_f32_e32 v36, v36, v37
	v_mul_f32_e32 v36, 0x41000000, v36
	v_mov_b32_e32 v37, 0
	v_cvt_pk_fp8_f32 v37, v36, v36
	s_mov_b32 s26, 0x3593b000
	v_add_co_u32_e64 v34, s[26:27], s26, v34
	s_nop 1
	v_addc_co_u32_e64 v35, s[26:27], 0, v35, s[26:27]
	global_store_byte v[34:35], v37, off offset:2048
	s_cbranch_scc1 .LBB0_1998
.LBB0_2009:
	v_lshl_add_u64 v[36:37], s[46:47], 0, v[108:109]
	s_mov_b32 s26, 0x11b39000
	v_add_co_u32_e64 v38, s[26:27], s26, v36
	s_bitcmp1_b32 s61, 0
	s_nop 0
	v_addc_co_u32_e64 v39, s[26:27], 0, v37, s[26:27]
	s_mov_b32 s26, 0x11b3a000
	s_nop 0
	v_add_co_u32_e64 v36, s[26:27], s26, v36
	v_lshl_add_u64 v[34:35], s[46:47], 0, v[102:103]
	s_nop 0
	v_addc_co_u32_e64 v37, s[26:27], 0, v37, s[26:27]
	s_cselect_b32 s26, 0x3000, 0
	s_nop 0
	v_add_u32_e32 v45, s26, v115
	ds_read_u16 v40, v45 offset:33792
	ds_read_u16 v41, v45 offset:34048
	ds_read_u16 v42, v45 offset:34304
	ds_read_u16 v43, v45 offset:34560
	ds_read_u16 v44, v45 offset:34816
	ds_read_u16 v46, v45 offset:35072
	ds_read_u16 v47, v45 offset:35328
	ds_read_u16 v48, v45 offset:35584
	s_waitcnt lgkmcnt(7)
	v_cvt_f32_f16_e32 v40, v40
	global_load_ushort v148, v[34:35], off
	global_load_ushort v147, v[38:39], off offset:1024
	global_load_ushort v146, v[38:39], off offset:3072
	global_load_ushort v145, v[36:37], off offset:1024
	s_waitcnt lgkmcnt(6)
	v_cvt_f32_f16_e32 v34, v41
	s_waitcnt lgkmcnt(5)
	v_cvt_f32_f16_e32 v35, v42
	v_add_f32_e32 v36, 0, v40
	s_waitcnt lgkmcnt(4)
	v_cvt_f32_f16_e32 v37, v43
	v_add_f32_e32 v34, v36, v34
	v_add_f32_e32 v35, v34, v35
	s_waitcnt lgkmcnt(3)
	v_cvt_f32_f16_e32 v34, v44
	s_waitcnt lgkmcnt(2)
	v_cvt_f32_f16_e32 v38, v46
	s_waitcnt lgkmcnt(1)
	v_cvt_f32_f16_e32 v40, v47
	v_add_f32_e32 v36, v35, v37
	s_waitcnt lgkmcnt(0)
	v_cvt_f32_f16_e32 v42, v48
	v_cndmask_b32_e64 v35, 0, v36, s[10:11]
	v_cndmask_b32_e64 v37, 0, v34, s[12:13]
	v_add_f32_e32 v35, v35, v37
	v_cndmask_b32_e64 v37, 0, v38, s[12:13]
	v_add_f32_e32 v35, v35, v37
	v_cndmask_b32_e64 v37, 0, v40, s[12:13]
	v_add_f32_e32 v35, v35, v37
	v_cndmask_b32_e64 v37, 0, v42, s[12:13]
	v_add_f32_e32 v37, v35, v37
	ds_read_u16 v35, v45 offset:35840
	ds_read_u16 v39, v45 offset:36096
	ds_read_u16 v41, v45 offset:36352
	ds_read_u16 v43, v45 offset:36608
	ds_read_u16 v47, v45 offset:36864
	ds_read_u16 v49, v45 offset:37120
	ds_read_u16 v51, v45 offset:37376
	ds_read_u16 v52, v45 offset:37632
	s_waitcnt lgkmcnt(7)
	v_cvt_f32_f16_e32 v44, v35
	s_waitcnt lgkmcnt(6)
	v_cvt_f32_f16_e32 v46, v39
	s_waitcnt lgkmcnt(5)
	v_cvt_f32_f16_e32 v48, v41
	s_waitcnt lgkmcnt(4)
	v_cvt_f32_f16_e32 v50, v43
	v_cndmask_b32_e64 v35, 0, v44, s[14:15]
	v_cndmask_b32_e64 v39, 0, v46, s[14:15]
	v_add_f32_e32 v34, v36, v34
	v_add_f32_e32 v35, v37, v35
	s_waitcnt lgkmcnt(3)
	v_cvt_f32_f16_e32 v36, v47
	v_cndmask_b32_e64 v41, 0, v48, s[14:15]
	v_add_f32_e32 v34, v34, v38
	v_add_f32_e32 v35, v35, v39
	s_waitcnt lgkmcnt(2)
	v_cvt_f32_f16_e32 v38, v49
	v_cndmask_b32_e64 v43, 0, v50, s[14:15]
	v_add_u32_e32 v53, v45, v111
	v_add_f32_e32 v34, v34, v40
	v_add_f32_e32 v35, v35, v41
	s_waitcnt lgkmcnt(1)
	v_cvt_f32_f16_e32 v40, v51
	ds_read_u16 v45, v53 offset:41984
	ds_read_u16 v54, v53 offset:33792
	ds_read_u16 v55, v53 offset:34048
	ds_read_u16 v56, v53 offset:34304
	ds_read_u16 v57, v53 offset:34560
	v_add_f32_e32 v34, v34, v42
	v_add_f32_e32 v35, v35, v43
	s_waitcnt lgkmcnt(5)
	v_cvt_f32_f16_e32 v42, v52
	s_waitcnt lgkmcnt(4)
	v_lshlrev_b32_e32 v58, 16, v45
	v_cndmask_b32_e64 v45, 0, v36, s[16:17]
	s_waitcnt lgkmcnt(3)
	v_cvt_f32_f16_e32 v37, v54
	v_add_f32_e32 v34, v34, v44
	v_add_f32_e32 v35, v35, v45
	v_cndmask_b32_e64 v47, 0, v38, s[16:17]
	v_add_f32_e32 v34, v34, v46
	v_add_f32_e32 v35, v35, v47
	v_cndmask_b32_e64 v49, 0, v40, s[16:17]
	v_add_f32_e32 v34, v34, v48
	v_add_f32_e32 v35, v35, v49
	v_cndmask_b32_e64 v51, 0, v42, s[16:17]
	v_add_f32_e32 v34, v34, v50
	v_add_f32_e32 v35, v35, v51
	s_waitcnt lgkmcnt(2)
	v_cvt_f32_f16_e32 v39, v55
	v_add_f32_e32 v44, v34, v36
	v_add_f32_e32 v45, v35, v37
	s_waitcnt lgkmcnt(1)
	v_cvt_f32_f16_e32 v41, v56
	v_mul_f32_e32 v34, 0x3fb8aa3b, v45
	v_exp_f32_e32 v34, v34
	v_mul_f32_e32 v35, 0x3fb8aa3b, v37
	s_waitcnt lgkmcnt(0)
	v_cvt_f32_f16_e32 v43, v57
	v_exp_f32_e32 v36, v35
	v_min_f32_e64 v35, -v45, s52
	v_mul_f32_e32 v34, v34, v58
	v_mul_f32_e32 v35, 0x3fb8aa3b, v35
	v_exp_f32_e32 v50, v35
	v_bfe_u32 v35, v34, 16, 1
	v_add_f32_e32 v46, v44, v38
	v_add_f32_e32 v47, v45, v39
	v_add3_u32 v34, v34, v35, s53
	v_add_f32_e32 v48, v46, v40
	v_add_f32_e32 v49, v47, v41
	ds_write_b16_d16_hi v117, v34
	v_add_f32_e32 v34, v48, v42
	v_add_f32_e32 v35, v49, v43
	s_nop 0
	v_sub_f32_e32 v37, v34, v45
	v_mul_f32_e32 v37, 0x3fb8aa3b, v37
	v_exp_f32_e32 v38, v37
	v_mul_f32_e32 v37, 0x3fb8aa3b, v39
	v_exp_f32_e32 v40, v37
	v_mul_f32_e32 v37, 0x3fb8aa3b, v47
	v_exp_f32_e32 v44, v37
	v_min_f32_e64 v37, -v47, s52
	v_mul_f32_e32 v37, 0x3fb8aa3b, v37
	v_exp_f32_e32 v45, v37
	v_sub_f32_e32 v37, v34, v47
	v_mul_f32_e32 v37, 0x3fb8aa3b, v37
	v_exp_f32_e32 v42, v37
	v_mul_f32_e32 v37, 0x3fb8aa3b, v41
	v_exp_f32_e32 v37, v37
	v_mul_f32_e32 v39, 0x3fb8aa3b, v49
	v_exp_f32_e32 v46, v39
	v_min_f32_e64 v39, -v49, s52
	v_pk_add_f32 v[36:37], v[36:37], 1.0 op_sel_hi:[1,0] neg_lo:[1,0] neg_hi:[1,0]
	v_mul_f32_e32 v39, 0x3fb8aa3b, v39
	v_mul_f32_e32 v41, v36, v50
	v_bfe_u32 v48, v41, 16, 1
	v_add3_u32 v41, v41, v48, s53
	ds_write_b16_d16_hi v117, v41 offset:4096
	v_exp_f32_e32 v47, v39
	v_sub_f32_e32 v39, v34, v49
	ds_read_u16 v48, v53 offset:37888
	ds_read_u16 v49, v53 offset:42240
	v_mul_f32_e32 v41, 0x3fb8aa3b, v43
	v_exp_f32_e32 v41, v41
	v_mul_f32_e32 v43, 0x3fb8aa3b, v35
	v_exp_f32_e32 v50, v43
	s_waitcnt lgkmcnt(0)
	v_lshlrev_b32_e32 v43, 16, v49
	v_mul_f32_e32 v43, v44, v43
	v_pk_add_f32 v[40:41], v[40:41], 1.0 op_sel_hi:[1,0] neg_lo:[1,0] neg_hi:[1,0]
	v_mul_f32_e32 v39, 0x3fb8aa3b, v39
	v_mul_f32_e32 v44, v40, v45
	v_bfe_u32 v45, v43, 16, 1
	v_add3_u32 v43, v43, v45, s53
	ds_write_b16_d16_hi v118, v43 offset:256
	v_bfe_u32 v43, v44, 16, 1
	v_add3_u32 v43, v44, v43, s53
	ds_write_b16_d16_hi v118, v43 offset:4352
	ds_read_u16 v44, v53 offset:38144
	ds_read_u16 v43, v53 offset:42496
	v_min_f32_e64 v45, -v35, s52
	v_exp_f32_e32 v39, v39
	v_mul_f32_e32 v45, 0x3fb8aa3b, v45
	v_sub_f32_e32 v35, v34, v35
	s_waitcnt lgkmcnt(0)
	v_lshlrev_b32_e32 v43, 16, v43
	v_mul_f32_e32 v43, v46, v43
	v_mul_f32_e32 v46, v37, v47
	v_bfe_u32 v47, v43, 16, 1
	v_add3_u32 v43, v43, v47, s53
	ds_write_b16_d16_hi v119, v43 offset:512
	v_bfe_u32 v43, v46, 16, 1
	v_add3_u32 v43, v46, v43, s53
	ds_write_b16_d16_hi v119, v43 offset:4608
	ds_read_u16 v46, v53 offset:38400
	ds_read_u16 v47, v53 offset:42752
	v_exp_f32_e32 v45, v45
	v_mul_f32_e32 v35, 0x3fb8aa3b, v35
	v_exp_f32_e32 v43, v35
	v_mul_f32_e32 v36, v36, v38
	v_mul_f32_e32 v37, v37, v39
	s_waitcnt lgkmcnt(0)
	v_lshlrev_b32_e32 v35, 16, v47
	v_mul_f32_e32 v35, v50, v35
	v_bfe_u32 v39, v35, 16, 1
	v_mul_f32_e32 v38, v41, v45
	v_add3_u32 v35, v35, v39, s53
	ds_write_b16_d16_hi v120, v35 offset:768
	v_bfe_u32 v35, v38, 16, 1
	v_add3_u32 v35, v38, v35, s53
	ds_write_b16_d16_hi v120, v35 offset:4864
	ds_read_u16 v35, v53 offset:38656
	v_and_b32_sdwa v38, v37, v79 dst_sel:DWORD dst_unused:UNUSED_PAD src0_sel:WORD_1 src1_sel:DWORD
	v_and_b32_sdwa v39, v36, v79 dst_sel:DWORD dst_unused:UNUSED_PAD src0_sel:WORD_1 src1_sel:DWORD
	v_add3_u32 v39, v36, v39, s53
	v_add3_u32 v38, v37, v38, s53
	v_mul_f32_e32 v36, v40, v42
	v_mul_f32_e32 v37, v41, v43
	s_waitcnt lgkmcnt(0)
	v_lshl_or_b32 v45, v35, 16, v46
	v_and_b32_sdwa v35, v37, v79 dst_sel:DWORD dst_unused:UNUSED_PAD src0_sel:WORD_1 src1_sel:DWORD
	v_and_b32_sdwa v40, v36, v79 dst_sel:DWORD dst_unused:UNUSED_PAD src0_sel:WORD_1 src1_sel:DWORD
	v_add3_u32 v35, v37, v35, s53
	v_add3_u32 v36, v36, v40, s53
	v_and_b32_e32 v35, 0xffff0000, v35
	v_and_b32_e32 v36, 0xffff0000, v36
	v_lshl_or_b32 v44, v44, 16, v48
	v_or_b32_sdwa v37, v35, v38 dst_sel:DWORD dst_unused:UNUSED_PAD src0_sel:DWORD src1_sel:WORD_1
	v_or_b32_sdwa v36, v36, v39 dst_sel:DWORD dst_unused:UNUSED_PAD src0_sel:DWORD src1_sel:WORD_1
	ds_write2st64_b64 v121, v[36:37], v[44:45] offset0:16 offset1:32
	s_and_saveexec_b64 s[26:27], vcc
	s_cbranch_execz .LBB0_2011
	v_mul_f32_e32 v34, 0x3fb8aa3b, v34
	v_exp_f32_e32 v34, v34
	v_add_u32_e32 v35, 0, v81
	ds_write_b32 v35, v34 offset:24576
.LBB0_2011:
	s_or_b64 exec, exec, s[26:27]
	s_waitcnt lgkmcnt(0)
	s_barrier
	ds_read_b128 v[34:37], v122 offset:16384
	ds_read_b128 v[38:41], v123
	ds_read_b128 v[42:45], v123 offset:4096
	v_add_u32_e32 v162, v112, v113
	s_waitcnt lgkmcnt(0)
	v_mfma_f32_16x16x32_bf16 v[38:41], v[38:41], v[42:45], 0
	ds_read_b128 v[42:45], v124
	ds_read_b128 v[46:49], v124 offset:4096
	v_add_u32_e32 v149, 0, v80
	s_add_i32 s36, s61, 1
	s_waitcnt lgkmcnt(0)
	v_mfma_f32_16x16x32_bf16 v[38:41], v[42:45], v[46:49], v[38:41]
	ds_read_b128 v[42:45], v125
	ds_read_b128 v[46:49], v125 offset:4096
	s_bitcmp1_b32 s36, 0
	s_cselect_b32 s26, 0x3000, 0
	s_waitcnt lgkmcnt(0)
	v_mfma_f32_16x16x32_bf16 v[38:41], v[42:45], v[46:49], v[38:41]
	ds_read_b128 v[42:45], v126
	ds_read_b128 v[46:49], v126 offset:4096
	s_cmp_gt_u32 s61, 61
	s_waitcnt lgkmcnt(0)
	v_mfma_f32_16x16x32_bf16 v[38:41], v[42:45], v[46:49], v[38:41]
	s_nop 7
	v_cndmask_b32_e64 v38, v38, 0, s[18:19]
	v_bfe_u32 v42, v38, 16, 1
	v_add3_u32 v38, v38, v42, s53
	ds_write_b16_d16_hi v127, v38 offset:25088
	v_cndmask_b32_e64 v38, v39, 0, s[20:21]
	v_bfe_u32 v39, v38, 16, 1
	v_add3_u32 v38, v38, v39, s53
	ds_write_b16_d16_hi v128, v38 offset:25088
	v_cndmask_b32_e64 v38, v40, 0, s[22:23]
	v_bfe_u32 v39, v38, 16, 1
	v_add3_u32 v38, v38, v39, s53
	ds_write_b16_d16_hi v129, v38 offset:25088
	v_cndmask_b32_e64 v38, v41, 0, s[24:25]
	v_bfe_u32 v39, v38, 16, 1
	v_add3_u32 v38, v38, v39, s53
	ds_write_b16_d16_hi v130, v38 offset:25088
	ds_read_b64 v[38:39], v131
	ds_read_b64 v[40:41], v132
	v_cvt_pk_bf16_f32 v42, v2, v3
	v_cvt_pk_bf16_f32 v43, v4, v5
	v_cvt_pk_bf16_f32 v44, v6, v7
	v_cvt_pk_bf16_f32 v45, v8, v9
	ds_read_b64 v[46:47], v133
	ds_read_b64 v[48:49], v134
	v_cvt_pk_bf16_f32 v50, v10, v11
	v_cvt_pk_bf16_f32 v51, v12, v13
	v_cvt_pk_bf16_f32 v52, v14, v15
	v_cvt_pk_bf16_f32 v53, v16, v17
	ds_read_b64 v[54:55], v135
	ds_read_b64 v[56:57], v136
	v_cvt_pk_bf16_f32 v58, v18, v19
	v_cvt_pk_bf16_f32 v59, v20, v21
	v_cvt_pk_bf16_f32 v60, v22, v23
	v_cvt_pk_bf16_f32 v61, v24, v25
	ds_read_b64 v[62:63], v137
	ds_read_b64 v[64:65], v138
	v_cvt_pk_bf16_f32 v66, v26, v27
	v_cvt_pk_bf16_f32 v67, v28, v29
	v_cvt_pk_bf16_f32 v68, v30, v31
	v_cvt_pk_bf16_f32 v69, v32, v33
	ds_read_b128 v[158:161], v162 offset:8192
	ds_read_b128 v[70:73], v139 offset:25088
	ds_read_b128 v[154:157], v149 offset:24576
	s_waitcnt lgkmcnt(9)
	v_mfma_f32_16x16x32_bf16 v[38:41], v[38:41], v[42:45], 0
	s_waitcnt lgkmcnt(0)
	v_mul_f32_e32 v2, v2, v154
	v_mul_f32_e32 v3, v3, v155
	v_mul_f32_e32 v4, v4, v156
	v_mul_f32_e32 v5, v5, v157
	v_mfma_f32_16x16x32_bf16 v[38:41], v[46:49], v[50:53], v[38:41]
	s_nop 0
	v_mfma_f32_16x16x32_bf16 v[2:5], v[158:161], v[34:37], v[2:5]
	ds_read_b128 v[154:157], v149 offset:24640
	ds_read_b128 v[158:161], v162 offset:9216
	s_waitcnt lgkmcnt(1)
	v_mul_f32_e32 v6, v6, v154
	v_mul_f32_e32 v7, v7, v155
	v_mul_f32_e32 v8, v8, v156
	v_mul_f32_e32 v9, v9, v157
	v_mfma_f32_16x16x32_bf16 v[38:41], v[54:57], v[58:61], v[38:41]
	s_waitcnt lgkmcnt(0)
	v_mfma_f32_16x16x32_bf16 v[6:9], v[158:161], v[34:37], v[6:9]
	ds_read_b128 v[154:157], v149 offset:24704
	ds_read_b128 v[158:161], v162 offset:10240
	s_waitcnt lgkmcnt(1)
	v_mul_f32_e32 v10, v10, v154
	v_mul_f32_e32 v11, v11, v155
	v_mul_f32_e32 v12, v12, v156
	v_mul_f32_e32 v13, v13, v157
	v_mfma_f32_16x16x32_bf16 v[38:41], v[62:65], v[66:69], v[38:41]
	s_waitcnt lgkmcnt(0)
	v_mfma_f32_16x16x32_bf16 v[10:13], v[158:161], v[34:37], v[10:13]
	ds_read_b128 v[154:157], v149 offset:24768
	ds_read_b128 v[158:161], v162 offset:11264
	s_waitcnt lgkmcnt(1)
	v_mul_f32_e32 v14, v14, v154
	v_mul_f32_e32 v15, v15, v155
	v_mul_f32_e32 v16, v16, v156
	v_mul_f32_e32 v17, v17, v157
	s_waitcnt lgkmcnt(0)
	s_nop 0
	v_mfma_f32_16x16x32_bf16 v[14:17], v[158:161], v[34:37], v[14:17]
	ds_read_b128 v[154:157], v149 offset:24832
	ds_read_b128 v[158:161], v162 offset:12288
	s_waitcnt lgkmcnt(1)
	v_mul_f32_e32 v18, v18, v154
	v_mul_f32_e32 v19, v19, v155
	v_mul_f32_e32 v20, v20, v156
	v_mul_f32_e32 v21, v21, v157
	s_waitcnt lgkmcnt(0)
	s_nop 0
	v_mfma_f32_16x16x32_bf16 v[18:21], v[158:161], v[34:37], v[18:21]
	ds_read_b128 v[154:157], v149 offset:24896
	ds_read_b128 v[158:161], v162 offset:13312
	s_waitcnt lgkmcnt(1)
	v_mul_f32_e32 v22, v22, v154
	v_mul_f32_e32 v23, v23, v155
	v_mul_f32_e32 v24, v24, v156
	v_mul_f32_e32 v25, v25, v157
	s_waitcnt lgkmcnt(0)
	s_nop 0
	v_mfma_f32_16x16x32_bf16 v[22:25], v[158:161], v[34:37], v[22:25]
	ds_read_b128 v[154:157], v149 offset:24960
	ds_read_b128 v[158:161], v162 offset:14336
	s_waitcnt lgkmcnt(1)
	v_mul_f32_e32 v26, v26, v154
	v_mul_f32_e32 v27, v27, v155
	v_mul_f32_e32 v28, v28, v156
	v_mul_f32_e32 v29, v29, v157
	s_waitcnt lgkmcnt(0)
	s_nop 0
	v_mfma_f32_16x16x32_bf16 v[26:29], v[158:161], v[34:37], v[26:29]
	ds_read_b128 v[154:157], v149 offset:25024
	ds_read_b128 v[158:161], v162 offset:15360
	s_waitcnt lgkmcnt(1)
	v_mul_f32_e32 v30, v30, v154
	v_mul_f32_e32 v31, v31, v155
	v_mul_f32_e32 v32, v32, v156
	v_mul_f32_e32 v33, v33, v157
	s_waitcnt lgkmcnt(0)
	s_nop 0
	v_mfma_f32_16x16x32_bf16 v[30:33], v[158:161], v[34:37], v[30:33]
	v_mfma_f32_16x16x32_bf16 v[34:37], v[70:73], v[34:37], v[38:41]
	s_nop 2
	v_add_u32_e32 v38, s26, v110
	s_waitcnt vmcnt(5)
	ds_write2st64_b64 v38, v[96:97], v[98:99] offset0:66 offset1:74
	s_waitcnt vmcnt(4)
	ds_write_b64 v38, v[100:101] offset:41984
	s_cbranch_scc1 .LBB0_2013
	v_lshlrev_b64 v[38:39], 1, v[74:75]
	v_lshl_add_u64 v[40:41], s[42:43], 0, v[38:39]
	v_lshl_add_u64 v[42:43], s[58:59], 0, v[38:39]
	v_lshl_add_u64 v[38:39], s[64:65], 0, v[38:39]
	global_load_dwordx2 v[96:97], v[40:41], off
	global_load_dwordx2 v[98:99], v[42:43], off
	global_load_dwordx2 v[100:101], v[38:39], off
